# speedup vs baseline: 1.0362x; 1.0362x over previous
_Z16bilateral_kernelPKfS0_Pf:
	s_load_dwordx2 s[4:5], s[0:1], 0x0
	s_load_dwordx2 s[8:9], s[0:1], 0x10
	s_and_b32 s0, s2, 7
	s_mulk_i32 s0, 0x60
	s_lshr_b32 s1, s2, 3
	s_add_i32 s1, s0, s1
	s_lshr_b32 s0, s1, 6
	s_lshl_b32 s1, s1, 3
	s_and_b32 s10, s1, 0x1c0
	s_lshl_b32 s1, s2, 3
	s_nop 0
	s_and_b32 s11, s1, 0x1c0
	s_mov_b32 s1, 0
	s_lshl_b64 s[2:3], s[0:1], 20
	s_mov_b32 s20, 0xc05dfbe6
	s_mov_b32 s21, 0xc05dfbe6
	s_mov_b32 s22, 0xc0a8390e
	s_mov_b32 s23, 0xc0a8390e
	s_mov_b32 s24, 0xc08211a7
	s_mov_b32 s25, 0xc08211a7
	s_mov_b32 s26, 0xc0bb4cc1
	s_mov_b32 s27, 0xc0bb4cc1
	s_mov_b32 s28, 0xc0f487dc
	s_mov_b32 s29, 0xc0f487dc
	s_mov_b32 s30, 0x3e0bd796
	s_mov_b32 s31, 0x3e0bd796
	s_mov_b32 s32, 0x3f45a90c
	s_mov_b32 s33, 0x3f45a90c
	s_mov_b32 s34, 0x3fa5c782
	s_mov_b32 s35, 0x3fa5c782
	v_and_b32_e32 v110, 15, v0
	v_lshrrev_b32_e32 v107, 2, v0
	v_lshl_or_b32 v105, v110, 2, s11
	v_and_or_b32 v109, v107, 60, s10
	v_min_u32_e32 v108, 0x1fa, v105
	v_sub_u32_e64 v107, v105, 2 clamp
	v_add_u32_e32 v108, 4, v108
	s_nop 0
	v_cmp_eq_u32_e64 s[16:17], 0, v110
	v_cmp_eq_u32_e32 vcc, 15, v110
	s_nop 1
	v_cndmask_b32_e64 v107, v108, v107, s[16:17]
	s_or_b64 vcc, s[16:17], vcc
	v_lshlrev_b32_e32 v107, 2, v107
	v_mov_b32_e32 v108, 0x7ff00000
	s_nop 0
	v_cndmask_b32_e32 v104, v108, v107, vcc
	s_movk_i32 s18, 0x1fc
	v_cmp_eq_u32_e32 vcc, 0, v105
	v_cmp_eq_u32_e64 s[16:17], s18, v105
	v_lshlrev_b32_e32 v105, 2, v105
	s_waitcnt lgkmcnt(0)
	s_add_u32 s4, s4, s2
	s_addc_u32 s5, s5, s3
	s_and_b32 s5, s5, 0xffff
	s_mov_b32 s6, 0x100000
	s_mov_b32 s7, 0x20000
	s_add_u32 s12, s8, s2
	s_addc_u32 s13, s9, s3
	s_and_b32 s13, s13, 0xffff
	s_mov_b32 s14, 0x100000
	s_mov_b32 s15, 0x20000
	v_sub_u32_e64 v107, v109, 2 clamp
	v_lshlrev_b32_e32 v107, 11, v107
	v_add_u32_e32 v108, v107, v104
	v_add_u32_e32 v107, v107, v105
	s_nop 0
	buffer_load_dwordx2 v[0:1], v108, s[4:7], 0 offen nt
	buffer_load_dwordx2 v[6:7], v108, s[4:7], 0 offen nt
	buffer_load_dwordx4 v[2:5], v107, s[4:7], 0 offen nt sc1
	v_sub_u32_e64 v107, v109, 1 clamp
	v_lshlrev_b32_e32 v107, 11, v107
	v_add_u32_e32 v108, v107, v104
	v_add_u32_e32 v107, v107, v105
	s_nop 0
	buffer_load_dwordx2 v[8:9], v108, s[4:7], 0 offen nt
	buffer_load_dwordx2 v[14:15], v108, s[4:7], 0 offen nt
	buffer_load_dwordx4 v[10:13], v107, s[4:7], 0 offen nt sc1
	v_lshlrev_b32_e32 v107, 11, v109
	v_add_u32_e32 v108, v107, v104
	v_add_u32_e32 v106, v107, v105
	s_nop 0
	v_add_u32_e32 v111, 0x1000, v106
	buffer_load_dwordx2 v[16:17], v108, s[4:7], 0 offen nt
	buffer_load_dwordx2 v[22:23], v108, s[4:7], 0 offen nt
	buffer_load_dwordx4 v[18:21], v106, s[4:7], 0 offen nt sc1
	v_lshlrev_b32_e32 v107, 11, v109
	s_nop 0
	v_add_u32_e32 v107, 0x800, v107
	v_add_u32_e32 v108, v107, v104
	v_add_u32_e32 v107, v107, v105
	buffer_load_dwordx2 v[24:25], v108, s[4:7], 0 offen nt
	buffer_load_dwordx2 v[30:31], v108, s[4:7], 0 offen nt
	buffer_load_dwordx4 v[26:29], v107, s[4:7], 0 offen nt sc1
	v_lshlrev_b32_e32 v107, 11, v109
	s_nop 0
	v_add_u32_e32 v107, 0x1000, v107
	v_add_u32_e32 v108, v107, v104
	v_add_u32_e32 v107, v107, v105
	buffer_load_dwordx2 v[32:33], v108, s[4:7], 0 offen nt
	buffer_load_dwordx2 v[38:39], v108, s[4:7], 0 offen nt
	buffer_load_dwordx4 v[34:37], v107, s[4:7], 0 offen nt sc1
	v_lshlrev_b32_e32 v107, 11, v109
	s_nop 0
	v_add_u32_e32 v107, 0x1800, v107
	v_add_u32_e32 v108, v107, v104
	v_add_u32_e32 v107, v107, v105
	buffer_load_dwordx2 v[40:41], v108, s[4:7], 0 offen nt
	buffer_load_dwordx2 v[46:47], v108, s[4:7], 0 offen nt
	buffer_load_dwordx4 v[42:45], v107, s[4:7], 0 offen nt sc1
	v_min_u32_e32 v107, 0x1fb, v109
	v_lshlrev_b32_e32 v107, 11, v107
	s_nop 0
	v_add_u32_e32 v107, 0x2000, v107
	v_add_u32_e32 v108, v107, v104
	v_add_u32_e32 v107, v107, v105
	buffer_load_dwordx2 v[48:49], v108, s[4:7], 0 offen nt
	buffer_load_dwordx2 v[54:55], v108, s[4:7], 0 offen nt
	buffer_load_dwordx4 v[50:53], v107, s[4:7], 0 offen nt sc1
	v_min_u32_e32 v107, 0x1fa, v109
	v_lshlrev_b32_e32 v107, 11, v107
	s_nop 0
	v_add_u32_e32 v107, 0x2800, v107
	v_add_u32_e32 v108, v107, v104
	v_add_u32_e32 v107, v107, v105
	buffer_load_dwordx2 v[56:57], v108, s[4:7], 0 offen nt
	buffer_load_dwordx2 v[62:63], v108, s[4:7], 0 offen nt
	buffer_load_dwordx4 v[58:61], v107, s[4:7], 0 offen nt sc1
	s_waitcnt vmcnt(21)
	s_nop 0
	v_mov_b32_dpp v0, v4 row_shr:1 row_mask:0xf bank_mask:0xf
	v_mov_b32_dpp v1, v5 row_shr:1 row_mask:0xf bank_mask:0xf
	v_mov_b32_dpp v6, v2 row_shl:1 row_mask:0xf bank_mask:0xf
	v_mov_b32_dpp v7, v3 row_shl:1 row_mask:0xf bank_mask:0xf
	v_pk_mul_f32 v[2:3], v[2:3], s[32:33]
	v_pk_mul_f32 v[4:5], v[4:5], s[32:33]
	v_cndmask_b32_e64 v1, v1, v0, vcc
	v_cndmask_b32_e64 v6, v6, v7, s[16:17]
	v_pk_mul_f32 v[0:1], v[0:1], s[32:33]
	v_pk_mul_f32 v[6:7], v[6:7], s[32:33]
	s_waitcnt vmcnt(18)
	s_nop 0
	v_mov_b32_dpp v8, v12 row_shr:1 row_mask:0xf bank_mask:0xf
	v_mov_b32_dpp v9, v13 row_shr:1 row_mask:0xf bank_mask:0xf
	v_mov_b32_dpp v14, v10 row_shl:1 row_mask:0xf bank_mask:0xf
	v_mov_b32_dpp v15, v11 row_shl:1 row_mask:0xf bank_mask:0xf
	v_pk_mul_f32 v[10:11], v[10:11], s[32:33]
	v_pk_mul_f32 v[12:13], v[12:13], s[32:33]
	v_cndmask_b32_e64 v9, v9, v8, vcc
	v_cndmask_b32_e64 v14, v14, v15, s[16:17]
	v_pk_mul_f32 v[8:9], v[8:9], s[32:33]
	v_pk_mul_f32 v[14:15], v[14:15], s[32:33]
	s_waitcnt vmcnt(15)
	s_nop 0
	v_mov_b32_dpp v16, v20 row_shr:1 row_mask:0xf bank_mask:0xf
	v_mov_b32_dpp v17, v21 row_shr:1 row_mask:0xf bank_mask:0xf
	v_mov_b32_dpp v22, v18 row_shl:1 row_mask:0xf bank_mask:0xf
	v_mov_b32_dpp v23, v19 row_shl:1 row_mask:0xf bank_mask:0xf
	v_pk_mul_f32 v[18:19], v[18:19], s[32:33]
	v_pk_mul_f32 v[20:21], v[20:21], s[32:33]
	v_cndmask_b32_e64 v17, v17, v16, vcc
	v_cndmask_b32_e64 v22, v22, v23, s[16:17]
	v_pk_mul_f32 v[68:69], v[18:19], s[30:31]
	v_pk_mul_f32 v[70:71], v[20:21], s[30:31]
	v_pk_mul_f32 v[16:17], v[16:17], s[32:33]
	v_pk_mul_f32 v[22:23], v[22:23], s[32:33]
	v_mov_b32_e32 v64, s30
	v_mov_b32_e32 v65, s30
	v_mov_b32_e32 v66, s30
	v_mov_b32_e32 v67, s30
	s_setprio 3
	s_nop 0
	v_pk_add_f32 v[96:97], v[18:19], v[0:1] neg_lo:[0,1] neg_hi:[0,1]
	v_pk_add_f32 v[98:99], v[18:19], v[2:3] neg_lo:[0,1] neg_hi:[0,1]
	v_pk_add_f32 v[100:101], v[20:21], v[2:3] neg_lo:[0,1] neg_hi:[0,1]
	v_pk_add_f32 v[102:103], v[18:19], v[4:5] neg_lo:[0,1] neg_hi:[0,1]
	v_pk_fma_f32 v[96:97], v[96:97], v[96:97], s[28:29] neg_lo:[1,0,0] neg_hi:[1,0,0]
	v_pk_fma_f32 v[98:99], v[98:99], v[98:99], s[22:23] neg_lo:[1,0,0] neg_hi:[1,0,0]
	v_pk_fma_f32 v[100:101], v[100:101], v[100:101], s[28:29] neg_lo:[1,0,0] neg_hi:[1,0,0]
	v_pk_fma_f32 v[102:103], v[102:103], v[102:103], s[28:29] neg_lo:[1,0,0] neg_hi:[1,0,0]
	v_exp_f32_e32 v96, v96
	v_exp_f32_e32 v97, v97
	v_exp_f32_e32 v98, v98
	v_exp_f32_e32 v99, v99
	v_exp_f32_e32 v100, v100
	v_exp_f32_e32 v101, v101
	v_exp_f32_e32 v102, v102
	v_exp_f32_e32 v103, v103
	v_pk_add_f32 v[64:65], v[64:65], v[96:97]
	v_pk_fma_f32 v[68:69], v[96:97], v[0:1], v[68:69]
	v_pk_add_f32 v[66:67], v[66:67], v[100:101]
	v_pk_add_f32 v[64:65], v[64:65], v[98:99]
	v_pk_fma_f32 v[68:69], v[98:99], v[2:3], v[68:69]
	v_pk_fma_f32 v[70:71], v[100:101], v[2:3], v[70:71]
	v_pk_add_f32 v[64:65], v[64:65], v[102:103]
	v_pk_fma_f32 v[68:69], v[102:103], v[4:5], v[68:69]
	v_pk_add_f32 v[96:97], v[20:21], v[4:5] neg_lo:[0,1] neg_hi:[0,1]
	v_pk_add_f32 v[98:99], v[20:21], v[6:7] neg_lo:[0,1] neg_hi:[0,1]
	v_pk_add_f32 v[100:101], v[18:19], v[2:3] op_sel:[1,0] op_sel_hi:[0,1] neg_lo:[0,1] neg_hi:[0,1]
	v_pk_add_f32 v[102:103], v[20:21], v[4:5] op_sel:[1,0] op_sel_hi:[0,1] neg_lo:[0,1] neg_hi:[0,1]
	v_pk_fma_f32 v[96:97], v[96:97], v[96:97], s[22:23] neg_lo:[1,0,0] neg_hi:[1,0,0]
	v_pk_fma_f32 v[98:99], v[98:99], v[98:99], s[28:29] neg_lo:[1,0,0] neg_hi:[1,0,0]
	v_pk_fma_f32 v[100:101], v[100:101], v[100:101], s[26:27] neg_lo:[1,0,0] neg_hi:[1,0,0]
	v_pk_fma_f32 v[102:103], v[102:103], v[102:103], s[26:27] neg_lo:[1,0,0] neg_hi:[1,0,0]
	v_exp_f32_e32 v96, v96
	v_exp_f32_e32 v97, v97
	v_exp_f32_e32 v98, v98
	v_exp_f32_e32 v99, v99
	v_exp_f32_e32 v100, v100
	v_exp_f32_e32 v101, v101
	v_exp_f32_e32 v102, v102
	v_exp_f32_e32 v103, v103
	v_pk_add_f32 v[66:67], v[66:67], v[96:97]
	v_pk_fma_f32 v[70:71], v[96:97], v[4:5], v[70:71]
	v_pk_add_f32 v[64:65], v[64:65], v[100:101] op_sel:[0,1] op_sel_hi:[1,0]
	v_pk_add_f32 v[66:67], v[66:67], v[98:99]
	v_pk_fma_f32 v[70:71], v[98:99], v[6:7], v[70:71]
	v_pk_fma_f32 v[68:69], v[100:101], v[2:3], v[68:69] op_sel:[1,1,0] op_sel_hi:[0,0,1]
	v_pk_add_f32 v[66:67], v[66:67], v[102:103] op_sel:[0,1] op_sel_hi:[1,0]
	v_pk_fma_f32 v[70:71], v[102:103], v[4:5], v[70:71] op_sel:[1,1,0] op_sel_hi:[0,0,1]
	v_pk_add_f32 v[96:97], v[18:19], v[8:9] neg_lo:[0,1] neg_hi:[0,1]
	v_pk_add_f32 v[98:99], v[18:19], v[10:11] neg_lo:[0,1] neg_hi:[0,1]
	v_pk_add_f32 v[100:101], v[20:21], v[10:11] neg_lo:[0,1] neg_hi:[0,1]
	v_pk_add_f32 v[102:103], v[18:19], v[12:13] neg_lo:[0,1] neg_hi:[0,1]
	v_pk_fma_f32 v[96:97], v[96:97], v[96:97], s[26:27] neg_lo:[1,0,0] neg_hi:[1,0,0]
	v_pk_fma_f32 v[98:99], v[98:99], v[98:99], s[20:21] neg_lo:[1,0,0] neg_hi:[1,0,0]
	v_pk_fma_f32 v[100:101], v[100:101], v[100:101], s[26:27] neg_lo:[1,0,0] neg_hi:[1,0,0]
	v_pk_fma_f32 v[102:103], v[102:103], v[102:103], s[26:27] neg_lo:[1,0,0] neg_hi:[1,0,0]
	v_exp_f32_e32 v96, v96
	v_exp_f32_e32 v97, v97
	v_exp_f32_e32 v98, v98
	v_exp_f32_e32 v99, v99
	v_exp_f32_e32 v100, v100
	v_exp_f32_e32 v101, v101
	v_exp_f32_e32 v102, v102
	v_exp_f32_e32 v103, v103
	v_pk_add_f32 v[64:65], v[64:65], v[96:97]
	v_pk_fma_f32 v[68:69], v[96:97], v[8:9], v[68:69]
	v_pk_add_f32 v[66:67], v[66:67], v[100:101]
	v_pk_add_f32 v[64:65], v[64:65], v[98:99]
	v_pk_fma_f32 v[68:69], v[98:99], v[10:11], v[68:69]
	v_pk_fma_f32 v[70:71], v[100:101], v[10:11], v[70:71]
	v_pk_add_f32 v[64:65], v[64:65], v[102:103]
	v_pk_fma_f32 v[68:69], v[102:103], v[12:13], v[68:69]
	v_pk_add_f32 v[96:97], v[20:21], v[12:13] neg_lo:[0,1] neg_hi:[0,1]
	v_pk_add_f32 v[98:99], v[20:21], v[14:15] neg_lo:[0,1] neg_hi:[0,1]
	v_pk_add_f32 v[100:101], v[18:19], v[10:11] op_sel:[1,0] op_sel_hi:[0,1] neg_lo:[0,1] neg_hi:[0,1]
	v_pk_add_f32 v[102:103], v[20:21], v[12:13] op_sel:[1,0] op_sel_hi:[0,1] neg_lo:[0,1] neg_hi:[0,1]
	v_pk_fma_f32 v[96:97], v[96:97], v[96:97], s[20:21] neg_lo:[1,0,0] neg_hi:[1,0,0]
	v_pk_fma_f32 v[98:99], v[98:99], v[98:99], s[26:27] neg_lo:[1,0,0] neg_hi:[1,0,0]
	v_pk_fma_f32 v[100:101], v[100:101], v[100:101], s[24:25] neg_lo:[1,0,0] neg_hi:[1,0,0]
	v_pk_fma_f32 v[102:103], v[102:103], v[102:103], s[24:25] neg_lo:[1,0,0] neg_hi:[1,0,0]
	v_exp_f32_e32 v96, v96
	v_exp_f32_e32 v97, v97
	v_exp_f32_e32 v98, v98
	v_exp_f32_e32 v99, v99
	v_exp_f32_e32 v100, v100
	v_exp_f32_e32 v101, v101
	v_exp_f32_e32 v102, v102
	v_exp_f32_e32 v103, v103
	v_pk_add_f32 v[66:67], v[66:67], v[96:97]
	v_pk_fma_f32 v[70:71], v[96:97], v[12:13], v[70:71]
	v_pk_add_f32 v[64:65], v[64:65], v[100:101] op_sel:[0,1] op_sel_hi:[1,0]
	v_pk_add_f32 v[66:67], v[66:67], v[98:99]
	v_pk_fma_f32 v[70:71], v[98:99], v[14:15], v[70:71]
	v_pk_fma_f32 v[68:69], v[100:101], v[10:11], v[68:69] op_sel:[1,1,0] op_sel_hi:[0,0,1]
	v_pk_add_f32 v[66:67], v[66:67], v[102:103] op_sel:[0,1] op_sel_hi:[1,0]
	v_pk_fma_f32 v[70:71], v[102:103], v[12:13], v[70:71] op_sel:[1,1,0] op_sel_hi:[0,0,1]
	v_pk_add_f32 v[96:97], v[18:19], v[16:17] neg_lo:[0,1] neg_hi:[0,1]
	v_pk_add_f32 v[98:99], v[20:21], v[18:19] neg_lo:[0,1] neg_hi:[0,1]
	v_pk_add_f32 v[100:101], v[22:23], v[20:21] neg_lo:[0,1] neg_hi:[0,1]
	v_pk_fma_f32 v[96:97], v[96:97], v[96:97], s[22:23] neg_lo:[1,0,0] neg_hi:[1,0,0]
	v_pk_fma_f32 v[98:99], v[98:99], v[98:99], s[22:23] neg_lo:[1,0,0] neg_hi:[1,0,0]
	v_pk_fma_f32 v[100:101], v[100:101], v[100:101], s[22:23] neg_lo:[1,0,0] neg_hi:[1,0,0]
	v_exp_f32_e32 v96, v96
	v_exp_f32_e32 v97, v97
	v_exp_f32_e32 v98, v98
	v_exp_f32_e32 v99, v99
	v_exp_f32_e32 v100, v100
	v_exp_f32_e32 v101, v101
	v_pk_add_f32 v[64:65], v[64:65], v[96:97]
	v_pk_fma_f32 v[68:69], v[96:97], v[16:17], v[68:69]
	v_pk_add_f32 v[66:67], v[66:67], v[98:99]
	v_pk_add_f32 v[64:65], v[64:65], v[98:99]
	v_pk_fma_f32 v[68:69], v[98:99], v[20:21], v[68:69]
	v_pk_fma_f32 v[70:71], v[98:99], v[18:19], v[70:71]
	v_pk_add_f32 v[66:67], v[66:67], v[100:101]
	v_pk_fma_f32 v[70:71], v[100:101], v[22:23], v[70:71]
	v_sub_f32_e32 v96, v18, v1
	v_sub_f32_e32 v98, v20, v3
	v_sub_f32_e32 v100, v19, v4
	v_sub_f32_e32 v102, v21, v6
	v_sub_f32_e32 v97, v18, v9
	v_sub_f32_e32 v99, v20, v11
	v_sub_f32_e32 v101, v19, v12
	v_sub_f32_e32 v103, v21, v14
	v_fma_f32 v96, -v96, v96, s26
	v_fma_f32 v98, -v98, v98, s26
	v_fma_f32 v100, -v100, v100, s26
	v_fma_f32 v102, -v102, v102, s26
	v_fma_f32 v97, -v97, v97, s24
	v_fma_f32 v99, -v99, v99, s24
	v_fma_f32 v101, -v101, v101, s24
	v_fma_f32 v103, -v103, v103, s24
	v_exp_f32_e32 v96, v96
	v_exp_f32_e32 v98, v98
	v_exp_f32_e32 v100, v100
	v_exp_f32_e32 v102, v102
	v_exp_f32_e32 v97, v97
	v_exp_f32_e32 v99, v99
	v_exp_f32_e32 v101, v101
	v_exp_f32_e32 v103, v103
	v_add_f32_e32 v64, v64, v96
	v_fmac_f32_e32 v68, v96, v1
	v_add_f32_e32 v66, v66, v98
	v_fmac_f32_e32 v70, v98, v3
	v_add_f32_e32 v65, v65, v100
	v_fmac_f32_e32 v69, v100, v4
	v_add_f32_e32 v67, v67, v102
	v_fmac_f32_e32 v71, v102, v6
	v_add_f32_e32 v64, v64, v97
	v_fmac_f32_e32 v68, v97, v9
	v_add_f32_e32 v66, v66, v99
	v_fmac_f32_e32 v70, v99, v11
	v_add_f32_e32 v65, v65, v101
	v_fmac_f32_e32 v69, v101, v12
	v_add_f32_e32 v67, v67, v103
	v_fmac_f32_e32 v71, v103, v14
	v_sub_f32_e32 v100, v18, v17
	v_sub_f32_e32 v96, v19, v18
	v_sub_f32_e32 v102, v20, v19
	v_sub_f32_e32 v98, v21, v20
	v_sub_f32_e32 v97, v22, v21
	s_nop 0
	v_fma_f32 v100, -v100, v100, s20
	v_fma_f32 v96, -v96, v96, s20
	v_fma_f32 v102, -v102, v102, s20
	v_fma_f32 v98, -v98, v98, s20
	v_fma_f32 v97, -v97, v97, s20
	v_exp_f32_e32 v100, v100
	v_exp_f32_e32 v96, v96
	v_exp_f32_e32 v102, v102
	v_exp_f32_e32 v98, v98
	v_exp_f32_e32 v97, v97
	v_add_f32_e32 v64, v64, v100
	v_fmac_f32_e32 v68, v100, v17
	v_add_f32_e32 v65, v65, v102
	v_fmac_f32_e32 v69, v102, v20
	v_add_f32_e32 v66, v66, v102
	v_fmac_f32_e32 v70, v102, v19
	v_add_f32_e32 v67, v67, v97
	v_fmac_f32_e32 v71, v97, v22
	s_nop 0
	v_pk_add_f32 v[64:65], v[64:65], v[96:97] op_sel_hi:[1,0]
	v_pk_fma_f32 v[68:69], v[96:97], v[18:19], v[68:69] op_sel:[0,1,0] op_sel_hi:[0,0,1]
	v_pk_add_f32 v[66:67], v[66:67], v[98:99] op_sel_hi:[1,0]
	v_pk_fma_f32 v[70:71], v[98:99], v[20:21], v[70:71] op_sel:[0,1,0] op_sel_hi:[0,0,1]
	s_waitcnt vmcnt(12)
	s_nop 0
	v_mov_b32_dpp v24, v28 row_shr:1 row_mask:0xf bank_mask:0xf
	v_mov_b32_dpp v25, v29 row_shr:1 row_mask:0xf bank_mask:0xf
	v_mov_b32_dpp v30, v26 row_shl:1 row_mask:0xf bank_mask:0xf
	v_mov_b32_dpp v31, v27 row_shl:1 row_mask:0xf bank_mask:0xf
	v_pk_mul_f32 v[26:27], v[26:27], s[32:33]
	v_pk_mul_f32 v[28:29], v[28:29], s[32:33]
	v_cndmask_b32_e64 v25, v25, v24, vcc
	v_cndmask_b32_e64 v30, v30, v31, s[16:17]
	v_pk_mul_f32 v[76:77], v[26:27], s[30:31]
	v_pk_mul_f32 v[78:79], v[28:29], s[30:31]
	v_pk_mul_f32 v[24:25], v[24:25], s[32:33]
	v_pk_mul_f32 v[30:31], v[30:31], s[32:33]
	v_mov_b32_e32 v72, s30
	v_mov_b32_e32 v73, s30
	v_mov_b32_e32 v74, s30
	v_mov_b32_e32 v75, s30
	s_setprio 3
	s_nop 0
	v_pk_add_f32 v[96:97], v[26:27], v[8:9] neg_lo:[0,1] neg_hi:[0,1]
	v_pk_add_f32 v[98:99], v[26:27], v[10:11] neg_lo:[0,1] neg_hi:[0,1]
	v_pk_add_f32 v[100:101], v[28:29], v[10:11] neg_lo:[0,1] neg_hi:[0,1]
	v_pk_add_f32 v[102:103], v[26:27], v[12:13] neg_lo:[0,1] neg_hi:[0,1]
	v_pk_fma_f32 v[96:97], v[96:97], v[96:97], s[28:29] neg_lo:[1,0,0] neg_hi:[1,0,0]
	v_pk_fma_f32 v[98:99], v[98:99], v[98:99], s[22:23] neg_lo:[1,0,0] neg_hi:[1,0,0]
	v_pk_fma_f32 v[100:101], v[100:101], v[100:101], s[28:29] neg_lo:[1,0,0] neg_hi:[1,0,0]
	v_pk_fma_f32 v[102:103], v[102:103], v[102:103], s[28:29] neg_lo:[1,0,0] neg_hi:[1,0,0]
	v_exp_f32_e32 v96, v96
	v_exp_f32_e32 v97, v97
	v_exp_f32_e32 v98, v98
	v_exp_f32_e32 v99, v99
	v_exp_f32_e32 v100, v100
	v_exp_f32_e32 v101, v101
	v_exp_f32_e32 v102, v102
	v_exp_f32_e32 v103, v103
	v_pk_add_f32 v[72:73], v[72:73], v[96:97]
	v_pk_fma_f32 v[76:77], v[96:97], v[8:9], v[76:77]
	v_pk_add_f32 v[74:75], v[74:75], v[100:101]
	v_pk_add_f32 v[72:73], v[72:73], v[98:99]
	v_pk_fma_f32 v[76:77], v[98:99], v[10:11], v[76:77]
	v_pk_fma_f32 v[78:79], v[100:101], v[10:11], v[78:79]
	v_pk_add_f32 v[72:73], v[72:73], v[102:103]
	v_pk_fma_f32 v[76:77], v[102:103], v[12:13], v[76:77]
	v_pk_add_f32 v[96:97], v[28:29], v[12:13] neg_lo:[0,1] neg_hi:[0,1]
	v_pk_add_f32 v[98:99], v[28:29], v[14:15] neg_lo:[0,1] neg_hi:[0,1]
	v_pk_add_f32 v[100:101], v[26:27], v[10:11] op_sel:[1,0] op_sel_hi:[0,1] neg_lo:[0,1] neg_hi:[0,1]
	v_pk_add_f32 v[102:103], v[28:29], v[12:13] op_sel:[1,0] op_sel_hi:[0,1] neg_lo:[0,1] neg_hi:[0,1]
	v_pk_fma_f32 v[96:97], v[96:97], v[96:97], s[22:23] neg_lo:[1,0,0] neg_hi:[1,0,0]
	v_pk_fma_f32 v[98:99], v[98:99], v[98:99], s[28:29] neg_lo:[1,0,0] neg_hi:[1,0,0]
	v_pk_fma_f32 v[100:101], v[100:101], v[100:101], s[26:27] neg_lo:[1,0,0] neg_hi:[1,0,0]
	v_pk_fma_f32 v[102:103], v[102:103], v[102:103], s[26:27] neg_lo:[1,0,0] neg_hi:[1,0,0]
	v_exp_f32_e32 v96, v96
	v_exp_f32_e32 v97, v97
	v_exp_f32_e32 v98, v98
	v_exp_f32_e32 v99, v99
	v_exp_f32_e32 v100, v100
	v_exp_f32_e32 v101, v101
	v_exp_f32_e32 v102, v102
	v_exp_f32_e32 v103, v103
	v_pk_add_f32 v[74:75], v[74:75], v[96:97]
	v_pk_fma_f32 v[78:79], v[96:97], v[12:13], v[78:79]
	v_pk_add_f32 v[72:73], v[72:73], v[100:101] op_sel:[0,1] op_sel_hi:[1,0]
	v_pk_add_f32 v[74:75], v[74:75], v[98:99]
	v_pk_fma_f32 v[78:79], v[98:99], v[14:15], v[78:79]
	v_pk_fma_f32 v[76:77], v[100:101], v[10:11], v[76:77] op_sel:[1,1,0] op_sel_hi:[0,0,1]
	v_pk_add_f32 v[74:75], v[74:75], v[102:103] op_sel:[0,1] op_sel_hi:[1,0]
	v_pk_fma_f32 v[78:79], v[102:103], v[12:13], v[78:79] op_sel:[1,1,0] op_sel_hi:[0,0,1]
	v_pk_add_f32 v[96:97], v[26:27], v[16:17] neg_lo:[0,1] neg_hi:[0,1]
	v_pk_add_f32 v[98:99], v[24:25], v[18:19] neg_lo:[0,1] neg_hi:[0,1]
	v_pk_add_f32 v[100:101], v[26:27], v[18:19] neg_lo:[0,1] neg_hi:[0,1]
	v_pk_add_f32 v[102:103], v[28:29], v[18:19] neg_lo:[0,1] neg_hi:[0,1]
	v_pk_fma_f32 v[96:97], v[96:97], v[96:97], s[26:27] neg_lo:[1,0,0] neg_hi:[1,0,0]
	v_pk_fma_f32 v[98:99], v[98:99], v[98:99], s[26:27] neg_lo:[1,0,0] neg_hi:[1,0,0]
	v_pk_fma_f32 v[100:101], v[100:101], v[100:101], s[20:21] neg_lo:[1,0,0] neg_hi:[1,0,0]
	v_pk_fma_f32 v[102:103], v[102:103], v[102:103], s[26:27] neg_lo:[1,0,0] neg_hi:[1,0,0]
	v_exp_f32_e32 v96, v96
	v_exp_f32_e32 v97, v97
	v_exp_f32_e32 v98, v98
	v_exp_f32_e32 v99, v99
	v_exp_f32_e32 v100, v100
	v_exp_f32_e32 v101, v101
	v_exp_f32_e32 v102, v102
	v_exp_f32_e32 v103, v103
	v_pk_add_f32 v[72:73], v[72:73], v[96:97]
	v_pk_fma_f32 v[76:77], v[96:97], v[16:17], v[76:77]
	v_pk_add_f32 v[64:65], v[64:65], v[98:99]
	v_pk_fma_f32 v[68:69], v[98:99], v[24:25], v[68:69]
	v_pk_add_f32 v[72:73], v[72:73], v[100:101]
	v_pk_add_f32 v[64:65], v[64:65], v[100:101]
	v_pk_fma_f32 v[68:69], v[100:101], v[26:27], v[68:69]
	v_pk_fma_f32 v[76:77], v[100:101], v[18:19], v[76:77]
	v_pk_add_f32 v[64:65], v[64:65], v[102:103]
	v_pk_fma_f32 v[68:69], v[102:103], v[28:29], v[68:69]
	v_pk_add_f32 v[74:75], v[74:75], v[102:103]
	v_pk_fma_f32 v[78:79], v[102:103], v[18:19], v[78:79]
	v_pk_add_f32 v[96:97], v[26:27], v[20:21] neg_lo:[0,1] neg_hi:[0,1]
	v_pk_add_f32 v[98:99], v[28:29], v[20:21] neg_lo:[0,1] neg_hi:[0,1]
	v_pk_add_f32 v[100:101], v[30:31], v[20:21] neg_lo:[0,1] neg_hi:[0,1]
	v_pk_add_f32 v[102:103], v[28:29], v[22:23] neg_lo:[0,1] neg_hi:[0,1]
	v_pk_fma_f32 v[96:97], v[96:97], v[96:97], s[26:27] neg_lo:[1,0,0] neg_hi:[1,0,0]
	v_pk_fma_f32 v[98:99], v[98:99], v[98:99], s[20:21] neg_lo:[1,0,0] neg_hi:[1,0,0]
	v_pk_fma_f32 v[100:101], v[100:101], v[100:101], s[26:27] neg_lo:[1,0,0] neg_hi:[1,0,0]
	v_pk_fma_f32 v[102:103], v[102:103], v[102:103], s[26:27] neg_lo:[1,0,0] neg_hi:[1,0,0]
	v_exp_f32_e32 v96, v96
	v_exp_f32_e32 v97, v97
	v_exp_f32_e32 v98, v98
	v_exp_f32_e32 v99, v99
	v_exp_f32_e32 v100, v100
	v_exp_f32_e32 v101, v101
	v_exp_f32_e32 v102, v102
	v_exp_f32_e32 v103, v103
	v_pk_add_f32 v[66:67], v[66:67], v[96:97]
	v_pk_fma_f32 v[70:71], v[96:97], v[26:27], v[70:71]
	v_pk_add_f32 v[72:73], v[72:73], v[96:97]
	v_pk_fma_f32 v[76:77], v[96:97], v[20:21], v[76:77]
	v_pk_add_f32 v[66:67], v[66:67], v[98:99]
	v_pk_fma_f32 v[70:71], v[98:99], v[28:29], v[70:71]
	v_pk_add_f32 v[74:75], v[74:75], v[98:99]
	v_pk_fma_f32 v[78:79], v[98:99], v[20:21], v[78:79]
	v_pk_add_f32 v[66:67], v[66:67], v[100:101]
	v_pk_fma_f32 v[70:71], v[100:101], v[30:31], v[70:71]
	v_pk_add_f32 v[74:75], v[74:75], v[102:103]
	v_pk_fma_f32 v[78:79], v[102:103], v[22:23], v[78:79]
	v_pk_add_f32 v[96:97], v[26:27], v[18:19] op_sel:[1,0] op_sel_hi:[0,1] neg_lo:[0,1] neg_hi:[0,1]
	v_pk_add_f32 v[98:99], v[28:29], v[20:21] op_sel:[1,0] op_sel_hi:[0,1] neg_lo:[0,1] neg_hi:[0,1]
	v_pk_add_f32 v[100:101], v[26:27], v[24:25] neg_lo:[0,1] neg_hi:[0,1]
	v_pk_add_f32 v[102:103], v[28:29], v[26:27] neg_lo:[0,1] neg_hi:[0,1]
	v_pk_fma_f32 v[96:97], v[96:97], v[96:97], s[24:25] neg_lo:[1,0,0] neg_hi:[1,0,0]
	v_pk_fma_f32 v[98:99], v[98:99], v[98:99], s[24:25] neg_lo:[1,0,0] neg_hi:[1,0,0]
	v_pk_fma_f32 v[100:101], v[100:101], v[100:101], s[22:23] neg_lo:[1,0,0] neg_hi:[1,0,0]
	v_pk_fma_f32 v[102:103], v[102:103], v[102:103], s[22:23] neg_lo:[1,0,0] neg_hi:[1,0,0]
	v_exp_f32_e32 v96, v96
	v_exp_f32_e32 v97, v97
	v_exp_f32_e32 v98, v98
	v_exp_f32_e32 v99, v99
	v_exp_f32_e32 v100, v100
	v_exp_f32_e32 v101, v101
	v_exp_f32_e32 v102, v102
	v_exp_f32_e32 v103, v103
	v_pk_add_f32 v[64:65], v[64:65], v[96:97]
	v_pk_fma_f32 v[68:69], v[96:97], v[26:27], v[68:69] op_sel:[0,1,0] op_sel_hi:[1,0,1]
	v_pk_add_f32 v[72:73], v[72:73], v[96:97] op_sel:[0,1] op_sel_hi:[1,0]
	v_pk_fma_f32 v[76:77], v[96:97], v[18:19], v[76:77] op_sel:[1,1,0] op_sel_hi:[0,0,1]
	v_pk_add_f32 v[66:67], v[66:67], v[98:99]
	v_pk_fma_f32 v[70:71], v[98:99], v[28:29], v[70:71] op_sel:[0,1,0] op_sel_hi:[1,0,1]
	v_pk_add_f32 v[74:75], v[74:75], v[98:99] op_sel:[0,1] op_sel_hi:[1,0]
	v_pk_fma_f32 v[78:79], v[98:99], v[20:21], v[78:79] op_sel:[1,1,0] op_sel_hi:[0,0,1]
	v_pk_add_f32 v[72:73], v[72:73], v[100:101]
	v_pk_fma_f32 v[76:77], v[100:101], v[24:25], v[76:77]
	v_pk_add_f32 v[74:75], v[74:75], v[102:103]
	v_pk_add_f32 v[72:73], v[72:73], v[102:103]
	v_pk_fma_f32 v[76:77], v[102:103], v[28:29], v[76:77]
	v_pk_fma_f32 v[78:79], v[102:103], v[26:27], v[78:79]
	v_pk_add_f32 v[96:97], v[30:31], v[28:29] neg_lo:[0,1] neg_hi:[0,1]
	v_pk_fma_f32 v[96:97], v[96:97], v[96:97], s[22:23] neg_lo:[1,0,0] neg_hi:[1,0,0]
	s_nop 0
	v_exp_f32_e32 v96, v96
	v_exp_f32_e32 v97, v97
	s_nop 0
	v_pk_add_f32 v[74:75], v[74:75], v[96:97]
	v_pk_fma_f32 v[78:79], v[96:97], v[30:31], v[78:79]
	v_sub_f32_e32 v96, v26, v9
	v_sub_f32_e32 v98, v28, v11
	v_sub_f32_e32 v100, v27, v12
	v_sub_f32_e32 v102, v29, v14
	v_sub_f32_e32 v97, v26, v17
	v_sub_f32_e32 v99, v25, v18
	v_sub_f32_e32 v101, v28, v19
	v_sub_f32_e32 v103, v27, v20
	v_fma_f32 v96, -v96, v96, s26
	v_fma_f32 v98, -v98, v98, s26
	v_fma_f32 v100, -v100, v100, s26
	v_fma_f32 v102, -v102, v102, s26
	v_fma_f32 v97, -v97, v97, s24
	v_fma_f32 v99, -v99, v99, s24
	v_fma_f32 v101, -v101, v101, s24
	v_fma_f32 v103, -v103, v103, s24
	v_exp_f32_e32 v96, v96
	v_exp_f32_e32 v98, v98
	v_exp_f32_e32 v100, v100
	v_exp_f32_e32 v102, v102
	v_exp_f32_e32 v97, v97
	v_exp_f32_e32 v99, v99
	v_exp_f32_e32 v101, v101
	v_exp_f32_e32 v103, v103
	v_add_f32_e32 v72, v72, v96
	v_fmac_f32_e32 v76, v96, v9
	v_add_f32_e32 v74, v74, v98
	v_fmac_f32_e32 v78, v98, v11
	v_add_f32_e32 v73, v73, v100
	v_fmac_f32_e32 v77, v100, v12
	v_add_f32_e32 v75, v75, v102
	v_fmac_f32_e32 v79, v102, v14
	v_add_f32_e32 v72, v72, v97
	v_fmac_f32_e32 v76, v97, v17
	v_add_f32_e32 v64, v64, v99
	v_fmac_f32_e32 v68, v99, v25
	v_add_f32_e32 v65, v65, v101
	v_fmac_f32_e32 v69, v101, v28
	v_add_f32_e32 v74, v74, v101
	v_fmac_f32_e32 v78, v101, v19
	v_add_f32_e32 v66, v66, v103
	v_fmac_f32_e32 v70, v103, v27
	v_add_f32_e32 v73, v73, v103
	v_fmac_f32_e32 v77, v103, v20
	v_sub_f32_e32 v100, v30, v21
	v_sub_f32_e32 v102, v29, v22
	v_sub_f32_e32 v97, v26, v25
	v_sub_f32_e32 v96, v27, v26
	v_sub_f32_e32 v99, v28, v27
	v_sub_f32_e32 v98, v29, v28
	v_sub_f32_e32 v101, v30, v29
	s_nop 0
	v_fma_f32 v100, -v100, v100, s24
	v_fma_f32 v102, -v102, v102, s24
	v_fma_f32 v97, -v97, v97, s20
	v_fma_f32 v96, -v96, v96, s20
	v_fma_f32 v99, -v99, v99, s20
	v_fma_f32 v98, -v98, v98, s20
	v_fma_f32 v101, -v101, v101, s20
	v_exp_f32_e32 v100, v100
	v_exp_f32_e32 v102, v102
	v_exp_f32_e32 v97, v97
	v_exp_f32_e32 v96, v96
	v_exp_f32_e32 v99, v99
	v_exp_f32_e32 v98, v98
	v_exp_f32_e32 v101, v101
	v_add_f32_e32 v67, v67, v100
	v_fmac_f32_e32 v71, v100, v30
	v_add_f32_e32 v75, v75, v102
	v_fmac_f32_e32 v79, v102, v22
	v_add_f32_e32 v72, v72, v97
	v_fmac_f32_e32 v76, v97, v25
	v_add_f32_e32 v73, v73, v99
	v_fmac_f32_e32 v77, v99, v28
	v_add_f32_e32 v74, v74, v99
	v_fmac_f32_e32 v78, v99, v27
	v_add_f32_e32 v75, v75, v101
	v_fmac_f32_e32 v79, v101, v30
	s_nop 0
	v_pk_add_f32 v[72:73], v[72:73], v[96:97] op_sel_hi:[1,0]
	v_pk_fma_f32 v[76:77], v[96:97], v[26:27], v[76:77] op_sel:[0,1,0] op_sel_hi:[0,0,1]
	v_pk_add_f32 v[74:75], v[74:75], v[98:99] op_sel_hi:[1,0]
	v_pk_fma_f32 v[78:79], v[98:99], v[28:29], v[78:79] op_sel:[0,1,0] op_sel_hi:[0,0,1]
	s_waitcnt vmcnt(9)
	s_nop 0
	v_mov_b32_dpp v32, v36 row_shr:1 row_mask:0xf bank_mask:0xf
	v_mov_b32_dpp v33, v37 row_shr:1 row_mask:0xf bank_mask:0xf
	v_mov_b32_dpp v38, v34 row_shl:1 row_mask:0xf bank_mask:0xf
	v_mov_b32_dpp v39, v35 row_shl:1 row_mask:0xf bank_mask:0xf
	v_pk_mul_f32 v[34:35], v[34:35], s[32:33]
	v_pk_mul_f32 v[36:37], v[36:37], s[32:33]
	v_cndmask_b32_e64 v33, v33, v32, vcc
	v_cndmask_b32_e64 v38, v38, v39, s[16:17]
	v_pk_mul_f32 v[84:85], v[34:35], s[30:31]
	v_pk_mul_f32 v[86:87], v[36:37], s[30:31]
	v_pk_mul_f32 v[32:33], v[32:33], s[32:33]
	v_pk_mul_f32 v[38:39], v[38:39], s[32:33]
	v_mov_b32_e32 v80, s30
	v_mov_b32_e32 v81, s30
	v_mov_b32_e32 v82, s30
	v_mov_b32_e32 v83, s30
	s_setprio 2
	s_nop 0
	v_pk_add_f32 v[96:97], v[34:35], v[16:17] neg_lo:[0,1] neg_hi:[0,1]
	v_pk_add_f32 v[98:99], v[32:33], v[18:19] neg_lo:[0,1] neg_hi:[0,1]
	v_pk_add_f32 v[100:101], v[34:35], v[18:19] neg_lo:[0,1] neg_hi:[0,1]
	v_pk_add_f32 v[102:103], v[36:37], v[18:19] neg_lo:[0,1] neg_hi:[0,1]
	v_pk_fma_f32 v[96:97], v[96:97], v[96:97], s[28:29] neg_lo:[1,0,0] neg_hi:[1,0,0]
	v_pk_fma_f32 v[98:99], v[98:99], v[98:99], s[28:29] neg_lo:[1,0,0] neg_hi:[1,0,0]
	v_pk_fma_f32 v[100:101], v[100:101], v[100:101], s[22:23] neg_lo:[1,0,0] neg_hi:[1,0,0]
	v_pk_fma_f32 v[102:103], v[102:103], v[102:103], s[28:29] neg_lo:[1,0,0] neg_hi:[1,0,0]
	v_exp_f32_e32 v96, v96
	v_exp_f32_e32 v97, v97
	v_exp_f32_e32 v98, v98
	v_exp_f32_e32 v99, v99
	v_exp_f32_e32 v100, v100
	v_exp_f32_e32 v101, v101
	v_exp_f32_e32 v102, v102
	v_exp_f32_e32 v103, v103
	v_pk_add_f32 v[80:81], v[80:81], v[96:97]
	v_pk_fma_f32 v[84:85], v[96:97], v[16:17], v[84:85]
	v_pk_add_f32 v[64:65], v[64:65], v[98:99]
	v_pk_fma_f32 v[68:69], v[98:99], v[32:33], v[68:69]
	v_pk_add_f32 v[80:81], v[80:81], v[100:101]
	v_pk_add_f32 v[64:65], v[64:65], v[100:101]
	v_pk_fma_f32 v[68:69], v[100:101], v[34:35], v[68:69]
	v_pk_fma_f32 v[84:85], v[100:101], v[18:19], v[84:85]
	v_pk_add_f32 v[64:65], v[64:65], v[102:103]
	v_pk_fma_f32 v[68:69], v[102:103], v[36:37], v[68:69]
	v_pk_add_f32 v[82:83], v[82:83], v[102:103]
	v_pk_fma_f32 v[86:87], v[102:103], v[18:19], v[86:87]
	v_pk_add_f32 v[96:97], v[34:35], v[20:21] neg_lo:[0,1] neg_hi:[0,1]
	v_pk_add_f32 v[98:99], v[36:37], v[20:21] neg_lo:[0,1] neg_hi:[0,1]
	v_pk_add_f32 v[100:101], v[38:39], v[20:21] neg_lo:[0,1] neg_hi:[0,1]
	v_pk_add_f32 v[102:103], v[36:37], v[22:23] neg_lo:[0,1] neg_hi:[0,1]
	v_pk_fma_f32 v[96:97], v[96:97], v[96:97], s[28:29] neg_lo:[1,0,0] neg_hi:[1,0,0]
	v_pk_fma_f32 v[98:99], v[98:99], v[98:99], s[22:23] neg_lo:[1,0,0] neg_hi:[1,0,0]
	v_pk_fma_f32 v[100:101], v[100:101], v[100:101], s[28:29] neg_lo:[1,0,0] neg_hi:[1,0,0]
	v_pk_fma_f32 v[102:103], v[102:103], v[102:103], s[28:29] neg_lo:[1,0,0] neg_hi:[1,0,0]
	v_exp_f32_e32 v96, v96
	v_exp_f32_e32 v97, v97
	v_exp_f32_e32 v98, v98
	v_exp_f32_e32 v99, v99
	v_exp_f32_e32 v100, v100
	v_exp_f32_e32 v101, v101
	v_exp_f32_e32 v102, v102
	v_exp_f32_e32 v103, v103
	v_pk_add_f32 v[66:67], v[66:67], v[96:97]
	v_pk_fma_f32 v[70:71], v[96:97], v[34:35], v[70:71]
	v_pk_add_f32 v[80:81], v[80:81], v[96:97]
	v_pk_fma_f32 v[84:85], v[96:97], v[20:21], v[84:85]
	v_pk_add_f32 v[66:67], v[66:67], v[98:99]
	v_pk_fma_f32 v[70:71], v[98:99], v[36:37], v[70:71]
	v_pk_add_f32 v[82:83], v[82:83], v[98:99]
	v_pk_fma_f32 v[86:87], v[98:99], v[20:21], v[86:87]
	v_pk_add_f32 v[66:67], v[66:67], v[100:101]
	v_pk_fma_f32 v[70:71], v[100:101], v[38:39], v[70:71]
	v_pk_add_f32 v[82:83], v[82:83], v[102:103]
	v_pk_fma_f32 v[86:87], v[102:103], v[22:23], v[86:87]
	v_pk_add_f32 v[96:97], v[34:35], v[18:19] op_sel:[1,0] op_sel_hi:[0,1] neg_lo:[0,1] neg_hi:[0,1]
	v_pk_add_f32 v[98:99], v[36:37], v[20:21] op_sel:[1,0] op_sel_hi:[0,1] neg_lo:[0,1] neg_hi:[0,1]
	v_pk_add_f32 v[100:101], v[34:35], v[24:25] neg_lo:[0,1] neg_hi:[0,1]
	v_pk_add_f32 v[102:103], v[32:33], v[26:27] neg_lo:[0,1] neg_hi:[0,1]
	v_pk_fma_f32 v[96:97], v[96:97], v[96:97], s[26:27] neg_lo:[1,0,0] neg_hi:[1,0,0]
	v_pk_fma_f32 v[98:99], v[98:99], v[98:99], s[26:27] neg_lo:[1,0,0] neg_hi:[1,0,0]
	v_pk_fma_f32 v[100:101], v[100:101], v[100:101], s[26:27] neg_lo:[1,0,0] neg_hi:[1,0,0]
	v_pk_fma_f32 v[102:103], v[102:103], v[102:103], s[26:27] neg_lo:[1,0,0] neg_hi:[1,0,0]
	v_exp_f32_e32 v96, v96
	v_exp_f32_e32 v97, v97
	v_exp_f32_e32 v98, v98
	v_exp_f32_e32 v99, v99
	v_exp_f32_e32 v100, v100
	v_exp_f32_e32 v101, v101
	v_exp_f32_e32 v102, v102
	v_exp_f32_e32 v103, v103
	v_pk_add_f32 v[64:65], v[64:65], v[96:97]
	v_pk_fma_f32 v[68:69], v[96:97], v[34:35], v[68:69] op_sel:[0,1,0] op_sel_hi:[1,0,1]
	v_pk_add_f32 v[80:81], v[80:81], v[96:97] op_sel:[0,1] op_sel_hi:[1,0]
	v_pk_fma_f32 v[84:85], v[96:97], v[18:19], v[84:85] op_sel:[1,1,0] op_sel_hi:[0,0,1]
	v_pk_add_f32 v[66:67], v[66:67], v[98:99]
	v_pk_fma_f32 v[70:71], v[98:99], v[36:37], v[70:71] op_sel:[0,1,0] op_sel_hi:[1,0,1]
	v_pk_add_f32 v[82:83], v[82:83], v[98:99] op_sel:[0,1] op_sel_hi:[1,0]
	v_pk_fma_f32 v[86:87], v[98:99], v[20:21], v[86:87] op_sel:[1,1,0] op_sel_hi:[0,0,1]
	v_pk_add_f32 v[80:81], v[80:81], v[100:101]
	v_pk_fma_f32 v[84:85], v[100:101], v[24:25], v[84:85]
	v_pk_add_f32 v[72:73], v[72:73], v[102:103]
	v_pk_fma_f32 v[76:77], v[102:103], v[32:33], v[76:77]
	v_pk_add_f32 v[96:97], v[34:35], v[26:27] neg_lo:[0,1] neg_hi:[0,1]
	v_pk_add_f32 v[98:99], v[36:37], v[26:27] neg_lo:[0,1] neg_hi:[0,1]
	v_pk_add_f32 v[100:101], v[34:35], v[28:29] neg_lo:[0,1] neg_hi:[0,1]
	v_pk_add_f32 v[102:103], v[36:37], v[28:29] neg_lo:[0,1] neg_hi:[0,1]
	v_pk_fma_f32 v[96:97], v[96:97], v[96:97], s[20:21] neg_lo:[1,0,0] neg_hi:[1,0,0]
	v_pk_fma_f32 v[98:99], v[98:99], v[98:99], s[26:27] neg_lo:[1,0,0] neg_hi:[1,0,0]
	v_pk_fma_f32 v[100:101], v[100:101], v[100:101], s[26:27] neg_lo:[1,0,0] neg_hi:[1,0,0]
	v_pk_fma_f32 v[102:103], v[102:103], v[102:103], s[20:21] neg_lo:[1,0,0] neg_hi:[1,0,0]
	v_exp_f32_e32 v96, v96
	v_exp_f32_e32 v97, v97
	v_exp_f32_e32 v98, v98
	v_exp_f32_e32 v99, v99
	v_exp_f32_e32 v100, v100
	v_exp_f32_e32 v101, v101
	v_exp_f32_e32 v102, v102
	v_exp_f32_e32 v103, v103
	v_pk_add_f32 v[72:73], v[72:73], v[96:97]
	v_pk_fma_f32 v[76:77], v[96:97], v[34:35], v[76:77]
	v_pk_add_f32 v[80:81], v[80:81], v[96:97]
	v_pk_fma_f32 v[84:85], v[96:97], v[26:27], v[84:85]
	v_pk_add_f32 v[72:73], v[72:73], v[98:99]
	v_pk_fma_f32 v[76:77], v[98:99], v[36:37], v[76:77]
	v_pk_add_f32 v[82:83], v[82:83], v[98:99]
	v_pk_fma_f32 v[86:87], v[98:99], v[26:27], v[86:87]
	v_pk_add_f32 v[74:75], v[74:75], v[100:101]
	v_pk_fma_f32 v[78:79], v[100:101], v[34:35], v[78:79]
	v_pk_add_f32 v[80:81], v[80:81], v[100:101]
	v_pk_fma_f32 v[84:85], v[100:101], v[28:29], v[84:85]
	v_pk_add_f32 v[74:75], v[74:75], v[102:103]
	v_pk_fma_f32 v[78:79], v[102:103], v[36:37], v[78:79]
	v_pk_add_f32 v[82:83], v[82:83], v[102:103]
	v_pk_fma_f32 v[86:87], v[102:103], v[28:29], v[86:87]
	v_pk_add_f32 v[96:97], v[38:39], v[28:29] neg_lo:[0,1] neg_hi:[0,1]
	v_pk_add_f32 v[98:99], v[36:37], v[30:31] neg_lo:[0,1] neg_hi:[0,1]
	v_pk_add_f32 v[100:101], v[34:35], v[26:27] op_sel:[1,0] op_sel_hi:[0,1] neg_lo:[0,1] neg_hi:[0,1]
	v_pk_add_f32 v[102:103], v[36:37], v[28:29] op_sel:[1,0] op_sel_hi:[0,1] neg_lo:[0,1] neg_hi:[0,1]
	v_pk_fma_f32 v[96:97], v[96:97], v[96:97], s[26:27] neg_lo:[1,0,0] neg_hi:[1,0,0]
	v_pk_fma_f32 v[98:99], v[98:99], v[98:99], s[26:27] neg_lo:[1,0,0] neg_hi:[1,0,0]
	v_pk_fma_f32 v[100:101], v[100:101], v[100:101], s[24:25] neg_lo:[1,0,0] neg_hi:[1,0,0]
	v_pk_fma_f32 v[102:103], v[102:103], v[102:103], s[24:25] neg_lo:[1,0,0] neg_hi:[1,0,0]
	v_exp_f32_e32 v96, v96
	v_exp_f32_e32 v97, v97
	v_exp_f32_e32 v98, v98
	v_exp_f32_e32 v99, v99
	v_exp_f32_e32 v100, v100
	v_exp_f32_e32 v101, v101
	v_exp_f32_e32 v102, v102
	v_exp_f32_e32 v103, v103
	v_pk_add_f32 v[74:75], v[74:75], v[96:97]
	v_pk_fma_f32 v[78:79], v[96:97], v[38:39], v[78:79]
	v_pk_add_f32 v[82:83], v[82:83], v[98:99]
	v_pk_fma_f32 v[86:87], v[98:99], v[30:31], v[86:87]
	v_pk_add_f32 v[72:73], v[72:73], v[100:101]
	v_pk_fma_f32 v[76:77], v[100:101], v[34:35], v[76:77] op_sel:[0,1,0] op_sel_hi:[1,0,1]
	v_pk_add_f32 v[80:81], v[80:81], v[100:101] op_sel:[0,1] op_sel_hi:[1,0]
	v_pk_fma_f32 v[84:85], v[100:101], v[26:27], v[84:85] op_sel:[1,1,0] op_sel_hi:[0,0,1]
	v_pk_add_f32 v[74:75], v[74:75], v[102:103]
	v_pk_fma_f32 v[78:79], v[102:103], v[36:37], v[78:79] op_sel:[0,1,0] op_sel_hi:[1,0,1]
	v_pk_add_f32 v[82:83], v[82:83], v[102:103] op_sel:[0,1] op_sel_hi:[1,0]
	v_pk_fma_f32 v[86:87], v[102:103], v[28:29], v[86:87] op_sel:[1,1,0] op_sel_hi:[0,0,1]
	v_pk_add_f32 v[96:97], v[34:35], v[32:33] neg_lo:[0,1] neg_hi:[0,1]
	v_pk_add_f32 v[98:99], v[36:37], v[34:35] neg_lo:[0,1] neg_hi:[0,1]
	v_pk_add_f32 v[100:101], v[38:39], v[36:37] neg_lo:[0,1] neg_hi:[0,1]
	v_pk_fma_f32 v[96:97], v[96:97], v[96:97], s[22:23] neg_lo:[1,0,0] neg_hi:[1,0,0]
	v_pk_fma_f32 v[98:99], v[98:99], v[98:99], s[22:23] neg_lo:[1,0,0] neg_hi:[1,0,0]
	v_pk_fma_f32 v[100:101], v[100:101], v[100:101], s[22:23] neg_lo:[1,0,0] neg_hi:[1,0,0]
	v_exp_f32_e32 v96, v96
	v_exp_f32_e32 v97, v97
	v_exp_f32_e32 v98, v98
	v_exp_f32_e32 v99, v99
	v_exp_f32_e32 v100, v100
	v_exp_f32_e32 v101, v101
	v_pk_add_f32 v[80:81], v[80:81], v[96:97]
	v_pk_fma_f32 v[84:85], v[96:97], v[32:33], v[84:85]
	v_pk_add_f32 v[82:83], v[82:83], v[98:99]
	v_pk_add_f32 v[80:81], v[80:81], v[98:99]
	v_pk_fma_f32 v[84:85], v[98:99], v[36:37], v[84:85]
	v_pk_fma_f32 v[86:87], v[98:99], v[34:35], v[86:87]
	v_pk_add_f32 v[82:83], v[82:83], v[100:101]
	v_pk_fma_f32 v[86:87], v[100:101], v[38:39], v[86:87]
	v_sub_f32_e32 v96, v34, v17
	v_sub_f32_e32 v98, v33, v18
	v_sub_f32_e32 v100, v36, v19
	v_sub_f32_e32 v102, v35, v20
	v_sub_f32_e32 v97, v38, v21
	v_sub_f32_e32 v99, v37, v22
	v_sub_f32_e32 v101, v34, v25
	v_sub_f32_e32 v103, v33, v26
	v_fma_f32 v96, -v96, v96, s26
	v_fma_f32 v98, -v98, v98, s26
	v_fma_f32 v100, -v100, v100, s26
	v_fma_f32 v102, -v102, v102, s26
	v_fma_f32 v97, -v97, v97, s26
	v_fma_f32 v99, -v99, v99, s26
	v_fma_f32 v101, -v101, v101, s24
	v_fma_f32 v103, -v103, v103, s24
	v_exp_f32_e32 v96, v96
	v_exp_f32_e32 v98, v98
	v_exp_f32_e32 v100, v100
	v_exp_f32_e32 v102, v102
	v_exp_f32_e32 v97, v97
	v_exp_f32_e32 v99, v99
	v_exp_f32_e32 v101, v101
	v_exp_f32_e32 v103, v103
	v_add_f32_e32 v80, v80, v96
	v_fmac_f32_e32 v84, v96, v17
	v_add_f32_e32 v64, v64, v98
	v_fmac_f32_e32 v68, v98, v33
	v_add_f32_e32 v65, v65, v100
	v_fmac_f32_e32 v69, v100, v36
	v_add_f32_e32 v82, v82, v100
	v_fmac_f32_e32 v86, v100, v19
	v_add_f32_e32 v66, v66, v102
	v_fmac_f32_e32 v70, v102, v35
	v_add_f32_e32 v81, v81, v102
	v_fmac_f32_e32 v85, v102, v20
	v_add_f32_e32 v67, v67, v97
	v_fmac_f32_e32 v71, v97, v38
	v_add_f32_e32 v83, v83, v99
	v_fmac_f32_e32 v87, v99, v22
	v_add_f32_e32 v80, v80, v101
	v_fmac_f32_e32 v84, v101, v25
	v_add_f32_e32 v72, v72, v103
	v_fmac_f32_e32 v76, v103, v33
	v_sub_f32_e32 v100, v36, v27
	v_sub_f32_e32 v102, v35, v28
	v_sub_f32_e32 v97, v38, v29
	v_sub_f32_e32 v99, v37, v30
	v_sub_f32_e32 v101, v34, v33
	v_sub_f32_e32 v96, v35, v34
	v_sub_f32_e32 v103, v36, v35
	v_sub_f32_e32 v98, v37, v36
	v_fma_f32 v100, -v100, v100, s24
	v_fma_f32 v102, -v102, v102, s24
	v_fma_f32 v97, -v97, v97, s24
	v_fma_f32 v99, -v99, v99, s24
	v_fma_f32 v101, -v101, v101, s20
	v_fma_f32 v96, -v96, v96, s20
	v_fma_f32 v103, -v103, v103, s20
	v_fma_f32 v98, -v98, v98, s20
	v_exp_f32_e32 v100, v100
	v_exp_f32_e32 v102, v102
	v_exp_f32_e32 v97, v97
	v_exp_f32_e32 v99, v99
	v_exp_f32_e32 v101, v101
	v_exp_f32_e32 v96, v96
	v_exp_f32_e32 v103, v103
	v_exp_f32_e32 v98, v98
	v_add_f32_e32 v73, v73, v100
	v_fmac_f32_e32 v77, v100, v36
	v_add_f32_e32 v82, v82, v100
	v_fmac_f32_e32 v86, v100, v27
	v_add_f32_e32 v74, v74, v102
	v_fmac_f32_e32 v78, v102, v35
	v_add_f32_e32 v81, v81, v102
	v_fmac_f32_e32 v85, v102, v28
	v_add_f32_e32 v75, v75, v97
	v_fmac_f32_e32 v79, v97, v38
	v_add_f32_e32 v83, v83, v99
	v_fmac_f32_e32 v87, v99, v30
	v_add_f32_e32 v80, v80, v101
	v_fmac_f32_e32 v84, v101, v33
	v_add_f32_e32 v81, v81, v103
	v_fmac_f32_e32 v85, v103, v36
	v_add_f32_e32 v82, v82, v103
	v_fmac_f32_e32 v86, v103, v35
	v_pk_add_f32 v[80:81], v[80:81], v[96:97] op_sel_hi:[1,0]
	v_pk_fma_f32 v[84:85], v[96:97], v[34:35], v[84:85] op_sel:[0,1,0] op_sel_hi:[0,0,1]
	v_pk_add_f32 v[82:83], v[82:83], v[98:99] op_sel_hi:[1,0]
	v_pk_fma_f32 v[86:87], v[98:99], v[36:37], v[86:87] op_sel:[0,1,0] op_sel_hi:[0,0,1]
	v_sub_f32_e32 v96, v38, v37
	s_nop 0
	v_fma_f32 v96, -v96, v96, s20
	s_nop 0
	v_exp_f32_e32 v96, v96
	s_nop 0
	v_add_f32_e32 v83, v83, v96
	v_fmac_f32_e32 v87, v96, v38
	s_nop 0
	v_rcp_f32_e32 v96, v64
	v_rcp_f32_e32 v97, v65
	v_rcp_f32_e32 v98, v66
	v_rcp_f32_e32 v99, v67
	v_pk_mul_f32 v[68:69], v[68:69], s[34:35]
	v_pk_mul_f32 v[70:71], v[70:71], s[34:35]
	v_pk_mul_f32 v[68:69], v[68:69], v[96:97]
	v_pk_mul_f32 v[70:71], v[70:71], v[98:99]
	s_nop 0
	s_nop 0
	buffer_store_dwordx4 v[68:71], v106, s[12:15], 0 offen sc1
	s_waitcnt vmcnt(7)
	s_nop 0
	v_mov_b32_dpp v40, v44 row_shr:1 row_mask:0xf bank_mask:0xf
	v_mov_b32_dpp v41, v45 row_shr:1 row_mask:0xf bank_mask:0xf
	v_mov_b32_dpp v46, v42 row_shl:1 row_mask:0xf bank_mask:0xf
	v_mov_b32_dpp v47, v43 row_shl:1 row_mask:0xf bank_mask:0xf
	v_pk_mul_f32 v[42:43], v[42:43], s[32:33]
	v_pk_mul_f32 v[44:45], v[44:45], s[32:33]
	v_cndmask_b32_e64 v41, v41, v40, vcc
	v_cndmask_b32_e64 v46, v46, v47, s[16:17]
	v_pk_mul_f32 v[92:93], v[42:43], s[30:31]
	v_pk_mul_f32 v[94:95], v[44:45], s[30:31]
	v_pk_mul_f32 v[40:41], v[40:41], s[32:33]
	v_pk_mul_f32 v[46:47], v[46:47], s[32:33]
	v_mov_b32_e32 v88, s30
	v_mov_b32_e32 v89, s30
	v_mov_b32_e32 v90, s30
	v_mov_b32_e32 v91, s30
	s_setprio 1
	s_nop 0
	v_pk_add_f32 v[96:97], v[42:43], v[24:25] neg_lo:[0,1] neg_hi:[0,1]
	v_pk_add_f32 v[98:99], v[40:41], v[26:27] neg_lo:[0,1] neg_hi:[0,1]
	v_pk_add_f32 v[100:101], v[42:43], v[26:27] neg_lo:[0,1] neg_hi:[0,1]
	v_pk_add_f32 v[102:103], v[44:45], v[26:27] neg_lo:[0,1] neg_hi:[0,1]
	v_pk_fma_f32 v[96:97], v[96:97], v[96:97], s[28:29] neg_lo:[1,0,0] neg_hi:[1,0,0]
	v_pk_fma_f32 v[98:99], v[98:99], v[98:99], s[28:29] neg_lo:[1,0,0] neg_hi:[1,0,0]
	v_pk_fma_f32 v[100:101], v[100:101], v[100:101], s[22:23] neg_lo:[1,0,0] neg_hi:[1,0,0]
	v_pk_fma_f32 v[102:103], v[102:103], v[102:103], s[28:29] neg_lo:[1,0,0] neg_hi:[1,0,0]
	v_exp_f32_e32 v96, v96
	v_exp_f32_e32 v97, v97
	v_exp_f32_e32 v98, v98
	v_exp_f32_e32 v99, v99
	v_exp_f32_e32 v100, v100
	v_exp_f32_e32 v101, v101
	v_exp_f32_e32 v102, v102
	v_exp_f32_e32 v103, v103
	v_pk_add_f32 v[88:89], v[88:89], v[96:97]
	v_pk_fma_f32 v[92:93], v[96:97], v[24:25], v[92:93]
	v_pk_add_f32 v[72:73], v[72:73], v[98:99]
	v_pk_fma_f32 v[76:77], v[98:99], v[40:41], v[76:77]
	v_pk_add_f32 v[88:89], v[88:89], v[100:101]
	v_pk_add_f32 v[72:73], v[72:73], v[100:101]
	v_pk_fma_f32 v[76:77], v[100:101], v[42:43], v[76:77]
	v_pk_fma_f32 v[92:93], v[100:101], v[26:27], v[92:93]
	v_pk_add_f32 v[72:73], v[72:73], v[102:103]
	v_pk_fma_f32 v[76:77], v[102:103], v[44:45], v[76:77]
	v_pk_add_f32 v[90:91], v[90:91], v[102:103]
	v_pk_fma_f32 v[94:95], v[102:103], v[26:27], v[94:95]
	v_pk_add_f32 v[96:97], v[42:43], v[28:29] neg_lo:[0,1] neg_hi:[0,1]
	v_pk_add_f32 v[98:99], v[44:45], v[28:29] neg_lo:[0,1] neg_hi:[0,1]
	v_pk_add_f32 v[100:101], v[46:47], v[28:29] neg_lo:[0,1] neg_hi:[0,1]
	v_pk_add_f32 v[102:103], v[44:45], v[30:31] neg_lo:[0,1] neg_hi:[0,1]
	v_pk_fma_f32 v[96:97], v[96:97], v[96:97], s[28:29] neg_lo:[1,0,0] neg_hi:[1,0,0]
	v_pk_fma_f32 v[98:99], v[98:99], v[98:99], s[22:23] neg_lo:[1,0,0] neg_hi:[1,0,0]
	v_pk_fma_f32 v[100:101], v[100:101], v[100:101], s[28:29] neg_lo:[1,0,0] neg_hi:[1,0,0]
	v_pk_fma_f32 v[102:103], v[102:103], v[102:103], s[28:29] neg_lo:[1,0,0] neg_hi:[1,0,0]
	v_exp_f32_e32 v96, v96
	v_exp_f32_e32 v97, v97
	v_exp_f32_e32 v98, v98
	v_exp_f32_e32 v99, v99
	v_exp_f32_e32 v100, v100
	v_exp_f32_e32 v101, v101
	v_exp_f32_e32 v102, v102
	v_exp_f32_e32 v103, v103
	v_pk_add_f32 v[74:75], v[74:75], v[96:97]
	v_pk_fma_f32 v[78:79], v[96:97], v[42:43], v[78:79]
	v_pk_add_f32 v[88:89], v[88:89], v[96:97]
	v_pk_fma_f32 v[92:93], v[96:97], v[28:29], v[92:93]
	v_pk_add_f32 v[74:75], v[74:75], v[98:99]
	v_pk_fma_f32 v[78:79], v[98:99], v[44:45], v[78:79]
	v_pk_add_f32 v[90:91], v[90:91], v[98:99]
	v_pk_fma_f32 v[94:95], v[98:99], v[28:29], v[94:95]
	v_pk_add_f32 v[74:75], v[74:75], v[100:101]
	v_pk_fma_f32 v[78:79], v[100:101], v[46:47], v[78:79]
	v_pk_add_f32 v[90:91], v[90:91], v[102:103]
	v_pk_fma_f32 v[94:95], v[102:103], v[30:31], v[94:95]
	v_pk_add_f32 v[96:97], v[42:43], v[26:27] op_sel:[1,0] op_sel_hi:[0,1] neg_lo:[0,1] neg_hi:[0,1]
	v_pk_add_f32 v[98:99], v[44:45], v[28:29] op_sel:[1,0] op_sel_hi:[0,1] neg_lo:[0,1] neg_hi:[0,1]
	v_pk_add_f32 v[100:101], v[42:43], v[32:33] neg_lo:[0,1] neg_hi:[0,1]
	v_pk_add_f32 v[102:103], v[40:41], v[34:35] neg_lo:[0,1] neg_hi:[0,1]
	v_pk_fma_f32 v[96:97], v[96:97], v[96:97], s[26:27] neg_lo:[1,0,0] neg_hi:[1,0,0]
	v_pk_fma_f32 v[98:99], v[98:99], v[98:99], s[26:27] neg_lo:[1,0,0] neg_hi:[1,0,0]
	v_pk_fma_f32 v[100:101], v[100:101], v[100:101], s[26:27] neg_lo:[1,0,0] neg_hi:[1,0,0]
	v_pk_fma_f32 v[102:103], v[102:103], v[102:103], s[26:27] neg_lo:[1,0,0] neg_hi:[1,0,0]
	v_exp_f32_e32 v96, v96
	v_exp_f32_e32 v97, v97
	v_exp_f32_e32 v98, v98
	v_exp_f32_e32 v99, v99
	v_exp_f32_e32 v100, v100
	v_exp_f32_e32 v101, v101
	v_exp_f32_e32 v102, v102
	v_exp_f32_e32 v103, v103
	v_pk_add_f32 v[72:73], v[72:73], v[96:97]
	v_pk_fma_f32 v[76:77], v[96:97], v[42:43], v[76:77] op_sel:[0,1,0] op_sel_hi:[1,0,1]
	v_pk_add_f32 v[88:89], v[88:89], v[96:97] op_sel:[0,1] op_sel_hi:[1,0]
	v_pk_fma_f32 v[92:93], v[96:97], v[26:27], v[92:93] op_sel:[1,1,0] op_sel_hi:[0,0,1]
	v_pk_add_f32 v[74:75], v[74:75], v[98:99]
	v_pk_fma_f32 v[78:79], v[98:99], v[44:45], v[78:79] op_sel:[0,1,0] op_sel_hi:[1,0,1]
	v_pk_add_f32 v[90:91], v[90:91], v[98:99] op_sel:[0,1] op_sel_hi:[1,0]
	v_pk_fma_f32 v[94:95], v[98:99], v[28:29], v[94:95] op_sel:[1,1,0] op_sel_hi:[0,0,1]
	v_pk_add_f32 v[88:89], v[88:89], v[100:101]
	v_pk_fma_f32 v[92:93], v[100:101], v[32:33], v[92:93]
	v_pk_add_f32 v[80:81], v[80:81], v[102:103]
	v_pk_fma_f32 v[84:85], v[102:103], v[40:41], v[84:85]
	v_pk_add_f32 v[96:97], v[42:43], v[34:35] neg_lo:[0,1] neg_hi:[0,1]
	v_pk_add_f32 v[98:99], v[44:45], v[34:35] neg_lo:[0,1] neg_hi:[0,1]
	v_pk_add_f32 v[100:101], v[42:43], v[36:37] neg_lo:[0,1] neg_hi:[0,1]
	v_pk_add_f32 v[102:103], v[44:45], v[36:37] neg_lo:[0,1] neg_hi:[0,1]
	v_pk_fma_f32 v[96:97], v[96:97], v[96:97], s[20:21] neg_lo:[1,0,0] neg_hi:[1,0,0]
	v_pk_fma_f32 v[98:99], v[98:99], v[98:99], s[26:27] neg_lo:[1,0,0] neg_hi:[1,0,0]
	v_pk_fma_f32 v[100:101], v[100:101], v[100:101], s[26:27] neg_lo:[1,0,0] neg_hi:[1,0,0]
	v_pk_fma_f32 v[102:103], v[102:103], v[102:103], s[20:21] neg_lo:[1,0,0] neg_hi:[1,0,0]
	v_exp_f32_e32 v96, v96
	v_exp_f32_e32 v97, v97
	v_exp_f32_e32 v98, v98
	v_exp_f32_e32 v99, v99
	v_exp_f32_e32 v100, v100
	v_exp_f32_e32 v101, v101
	v_exp_f32_e32 v102, v102
	v_exp_f32_e32 v103, v103
	v_pk_add_f32 v[80:81], v[80:81], v[96:97]
	v_pk_fma_f32 v[84:85], v[96:97], v[42:43], v[84:85]
	v_pk_add_f32 v[88:89], v[88:89], v[96:97]
	v_pk_fma_f32 v[92:93], v[96:97], v[34:35], v[92:93]
	v_pk_add_f32 v[80:81], v[80:81], v[98:99]
	v_pk_fma_f32 v[84:85], v[98:99], v[44:45], v[84:85]
	v_pk_add_f32 v[90:91], v[90:91], v[98:99]
	v_pk_fma_f32 v[94:95], v[98:99], v[34:35], v[94:95]
	v_pk_add_f32 v[82:83], v[82:83], v[100:101]
	v_pk_fma_f32 v[86:87], v[100:101], v[42:43], v[86:87]
	v_pk_add_f32 v[88:89], v[88:89], v[100:101]
	v_pk_fma_f32 v[92:93], v[100:101], v[36:37], v[92:93]
	v_pk_add_f32 v[82:83], v[82:83], v[102:103]
	v_pk_fma_f32 v[86:87], v[102:103], v[44:45], v[86:87]
	v_pk_add_f32 v[90:91], v[90:91], v[102:103]
	v_pk_fma_f32 v[94:95], v[102:103], v[36:37], v[94:95]
	v_pk_add_f32 v[96:97], v[46:47], v[36:37] neg_lo:[0,1] neg_hi:[0,1]
	v_pk_add_f32 v[98:99], v[44:45], v[38:39] neg_lo:[0,1] neg_hi:[0,1]
	v_pk_add_f32 v[100:101], v[42:43], v[34:35] op_sel:[1,0] op_sel_hi:[0,1] neg_lo:[0,1] neg_hi:[0,1]
	v_pk_add_f32 v[102:103], v[44:45], v[36:37] op_sel:[1,0] op_sel_hi:[0,1] neg_lo:[0,1] neg_hi:[0,1]
	v_pk_fma_f32 v[96:97], v[96:97], v[96:97], s[26:27] neg_lo:[1,0,0] neg_hi:[1,0,0]
	v_pk_fma_f32 v[98:99], v[98:99], v[98:99], s[26:27] neg_lo:[1,0,0] neg_hi:[1,0,0]
	v_pk_fma_f32 v[100:101], v[100:101], v[100:101], s[24:25] neg_lo:[1,0,0] neg_hi:[1,0,0]
	v_pk_fma_f32 v[102:103], v[102:103], v[102:103], s[24:25] neg_lo:[1,0,0] neg_hi:[1,0,0]
	v_exp_f32_e32 v96, v96
	v_exp_f32_e32 v97, v97
	v_exp_f32_e32 v98, v98
	v_exp_f32_e32 v99, v99
	v_exp_f32_e32 v100, v100
	v_exp_f32_e32 v101, v101
	v_exp_f32_e32 v102, v102
	v_exp_f32_e32 v103, v103
	v_pk_add_f32 v[82:83], v[82:83], v[96:97]
	v_pk_fma_f32 v[86:87], v[96:97], v[46:47], v[86:87]
	v_pk_add_f32 v[90:91], v[90:91], v[98:99]
	v_pk_fma_f32 v[94:95], v[98:99], v[38:39], v[94:95]
	v_pk_add_f32 v[80:81], v[80:81], v[100:101]
	v_pk_fma_f32 v[84:85], v[100:101], v[42:43], v[84:85] op_sel:[0,1,0] op_sel_hi:[1,0,1]
	v_pk_add_f32 v[88:89], v[88:89], v[100:101] op_sel:[0,1] op_sel_hi:[1,0]
	v_pk_fma_f32 v[92:93], v[100:101], v[34:35], v[92:93] op_sel:[1,1,0] op_sel_hi:[0,0,1]
	v_pk_add_f32 v[82:83], v[82:83], v[102:103]
	v_pk_fma_f32 v[86:87], v[102:103], v[44:45], v[86:87] op_sel:[0,1,0] op_sel_hi:[1,0,1]
	v_pk_add_f32 v[90:91], v[90:91], v[102:103] op_sel:[0,1] op_sel_hi:[1,0]
	v_pk_fma_f32 v[94:95], v[102:103], v[36:37], v[94:95] op_sel:[1,1,0] op_sel_hi:[0,0,1]
	v_pk_add_f32 v[96:97], v[42:43], v[40:41] neg_lo:[0,1] neg_hi:[0,1]
	v_pk_add_f32 v[98:99], v[44:45], v[42:43] neg_lo:[0,1] neg_hi:[0,1]
	v_pk_add_f32 v[100:101], v[46:47], v[44:45] neg_lo:[0,1] neg_hi:[0,1]
	v_pk_fma_f32 v[96:97], v[96:97], v[96:97], s[22:23] neg_lo:[1,0,0] neg_hi:[1,0,0]
	v_pk_fma_f32 v[98:99], v[98:99], v[98:99], s[22:23] neg_lo:[1,0,0] neg_hi:[1,0,0]
	v_pk_fma_f32 v[100:101], v[100:101], v[100:101], s[22:23] neg_lo:[1,0,0] neg_hi:[1,0,0]
	v_exp_f32_e32 v96, v96
	v_exp_f32_e32 v97, v97
	v_exp_f32_e32 v98, v98
	v_exp_f32_e32 v99, v99
	v_exp_f32_e32 v100, v100
	v_exp_f32_e32 v101, v101
	v_pk_add_f32 v[88:89], v[88:89], v[96:97]
	v_pk_fma_f32 v[92:93], v[96:97], v[40:41], v[92:93]
	v_pk_add_f32 v[90:91], v[90:91], v[98:99]
	v_pk_add_f32 v[88:89], v[88:89], v[98:99]
	v_pk_fma_f32 v[92:93], v[98:99], v[44:45], v[92:93]
	v_pk_fma_f32 v[94:95], v[98:99], v[42:43], v[94:95]
	v_pk_add_f32 v[90:91], v[90:91], v[100:101]
	v_pk_fma_f32 v[94:95], v[100:101], v[46:47], v[94:95]
	v_sub_f32_e32 v96, v42, v25
	v_sub_f32_e32 v98, v41, v26
	v_sub_f32_e32 v100, v44, v27
	v_sub_f32_e32 v102, v43, v28
	v_sub_f32_e32 v97, v46, v29
	v_sub_f32_e32 v99, v45, v30
	v_sub_f32_e32 v101, v42, v33
	v_sub_f32_e32 v103, v41, v34
	v_fma_f32 v96, -v96, v96, s26
	v_fma_f32 v98, -v98, v98, s26
	v_fma_f32 v100, -v100, v100, s26
	v_fma_f32 v102, -v102, v102, s26
	v_fma_f32 v97, -v97, v97, s26
	v_fma_f32 v99, -v99, v99, s26
	v_fma_f32 v101, -v101, v101, s24
	v_fma_f32 v103, -v103, v103, s24
	v_exp_f32_e32 v96, v96
	v_exp_f32_e32 v98, v98
	v_exp_f32_e32 v100, v100
	v_exp_f32_e32 v102, v102
	v_exp_f32_e32 v97, v97
	v_exp_f32_e32 v99, v99
	v_exp_f32_e32 v101, v101
	v_exp_f32_e32 v103, v103
	v_add_f32_e32 v88, v88, v96
	v_fmac_f32_e32 v92, v96, v25
	v_add_f32_e32 v72, v72, v98
	v_fmac_f32_e32 v76, v98, v41
	v_add_f32_e32 v73, v73, v100
	v_fmac_f32_e32 v77, v100, v44
	v_add_f32_e32 v90, v90, v100
	v_fmac_f32_e32 v94, v100, v27
	v_add_f32_e32 v74, v74, v102
	v_fmac_f32_e32 v78, v102, v43
	v_add_f32_e32 v89, v89, v102
	v_fmac_f32_e32 v93, v102, v28
	v_add_f32_e32 v75, v75, v97
	v_fmac_f32_e32 v79, v97, v46
	v_add_f32_e32 v91, v91, v99
	v_fmac_f32_e32 v95, v99, v30
	v_add_f32_e32 v88, v88, v101
	v_fmac_f32_e32 v92, v101, v33
	v_add_f32_e32 v80, v80, v103
	v_fmac_f32_e32 v84, v103, v41
	v_sub_f32_e32 v100, v44, v35
	v_sub_f32_e32 v102, v43, v36
	v_sub_f32_e32 v97, v46, v37
	v_sub_f32_e32 v99, v45, v38
	v_sub_f32_e32 v101, v42, v41
	v_sub_f32_e32 v96, v43, v42
	v_sub_f32_e32 v103, v44, v43
	v_sub_f32_e32 v98, v45, v44
	v_fma_f32 v100, -v100, v100, s24
	v_fma_f32 v102, -v102, v102, s24
	v_fma_f32 v97, -v97, v97, s24
	v_fma_f32 v99, -v99, v99, s24
	v_fma_f32 v101, -v101, v101, s20
	v_fma_f32 v96, -v96, v96, s20
	v_fma_f32 v103, -v103, v103, s20
	v_fma_f32 v98, -v98, v98, s20
	v_exp_f32_e32 v100, v100
	v_exp_f32_e32 v102, v102
	v_exp_f32_e32 v97, v97
	v_exp_f32_e32 v99, v99
	v_exp_f32_e32 v101, v101
	v_exp_f32_e32 v96, v96
	v_exp_f32_e32 v103, v103
	v_exp_f32_e32 v98, v98
	v_add_f32_e32 v81, v81, v100
	v_fmac_f32_e32 v85, v100, v44
	v_add_f32_e32 v90, v90, v100
	v_fmac_f32_e32 v94, v100, v35
	v_add_f32_e32 v82, v82, v102
	v_fmac_f32_e32 v86, v102, v43
	v_add_f32_e32 v89, v89, v102
	v_fmac_f32_e32 v93, v102, v36
	v_add_f32_e32 v83, v83, v97
	v_fmac_f32_e32 v87, v97, v46
	v_add_f32_e32 v91, v91, v99
	v_fmac_f32_e32 v95, v99, v38
	v_add_f32_e32 v88, v88, v101
	v_fmac_f32_e32 v92, v101, v41
	v_add_f32_e32 v89, v89, v103
	v_fmac_f32_e32 v93, v103, v44
	v_add_f32_e32 v90, v90, v103
	v_fmac_f32_e32 v94, v103, v43
	v_pk_add_f32 v[88:89], v[88:89], v[96:97] op_sel_hi:[1,0]
	v_pk_fma_f32 v[92:93], v[96:97], v[42:43], v[92:93] op_sel:[0,1,0] op_sel_hi:[0,0,1]
	v_pk_add_f32 v[90:91], v[90:91], v[98:99] op_sel_hi:[1,0]
	v_pk_fma_f32 v[94:95], v[98:99], v[44:45], v[94:95] op_sel:[0,1,0] op_sel_hi:[0,0,1]
	v_sub_f32_e32 v96, v46, v45
	s_nop 0
	v_fma_f32 v96, -v96, v96, s20
	s_nop 0
	v_exp_f32_e32 v96, v96
	s_nop 0
	v_add_f32_e32 v91, v91, v96
	v_fmac_f32_e32 v95, v96, v46
	s_nop 0
	v_rcp_f32_e32 v96, v72
	v_rcp_f32_e32 v97, v73
	v_rcp_f32_e32 v98, v74
	v_rcp_f32_e32 v99, v75
	v_pk_mul_f32 v[76:77], v[76:77], s[34:35]
	v_pk_mul_f32 v[78:79], v[78:79], s[34:35]
	v_pk_mul_f32 v[76:77], v[76:77], v[96:97]
	v_pk_mul_f32 v[78:79], v[78:79], v[98:99]
	s_nop 0
	s_nop 0
	buffer_store_dwordx4 v[76:79], v106, s[12:15], 0 offen offset:2048 sc1
	s_waitcnt vmcnt(5)
	s_nop 0
	v_mov_b32_dpp v48, v52 row_shr:1 row_mask:0xf bank_mask:0xf
	v_mov_b32_dpp v49, v53 row_shr:1 row_mask:0xf bank_mask:0xf
	v_mov_b32_dpp v54, v50 row_shl:1 row_mask:0xf bank_mask:0xf
	v_mov_b32_dpp v55, v51 row_shl:1 row_mask:0xf bank_mask:0xf
	v_pk_mul_f32 v[50:51], v[50:51], s[32:33]
	v_pk_mul_f32 v[52:53], v[52:53], s[32:33]
	v_cndmask_b32_e64 v49, v49, v48, vcc
	v_cndmask_b32_e64 v54, v54, v55, s[16:17]
	v_pk_mul_f32 v[48:49], v[48:49], s[32:33]
	v_pk_mul_f32 v[54:55], v[54:55], s[32:33]
	s_setprio 0
	s_nop 0
	v_pk_add_f32 v[96:97], v[48:49], v[34:35] neg_lo:[0,1] neg_hi:[0,1]
	v_pk_add_f32 v[98:99], v[50:51], v[34:35] neg_lo:[0,1] neg_hi:[0,1]
	v_pk_add_f32 v[100:101], v[52:53], v[34:35] neg_lo:[0,1] neg_hi:[0,1]
	v_pk_add_f32 v[102:103], v[50:51], v[36:37] neg_lo:[0,1] neg_hi:[0,1]
	v_pk_fma_f32 v[96:97], v[96:97], v[96:97], s[28:29] neg_lo:[1,0,0] neg_hi:[1,0,0]
	v_pk_fma_f32 v[98:99], v[98:99], v[98:99], s[22:23] neg_lo:[1,0,0] neg_hi:[1,0,0]
	v_pk_fma_f32 v[100:101], v[100:101], v[100:101], s[28:29] neg_lo:[1,0,0] neg_hi:[1,0,0]
	v_pk_fma_f32 v[102:103], v[102:103], v[102:103], s[28:29] neg_lo:[1,0,0] neg_hi:[1,0,0]
	v_exp_f32_e32 v96, v96
	v_exp_f32_e32 v97, v97
	v_exp_f32_e32 v98, v98
	v_exp_f32_e32 v99, v99
	v_exp_f32_e32 v100, v100
	v_exp_f32_e32 v101, v101
	v_exp_f32_e32 v102, v102
	v_exp_f32_e32 v103, v103
	v_pk_add_f32 v[80:81], v[80:81], v[96:97]
	v_pk_fma_f32 v[84:85], v[96:97], v[48:49], v[84:85]
	v_pk_add_f32 v[82:83], v[82:83], v[102:103]
	v_pk_add_f32 v[80:81], v[80:81], v[98:99]
	v_pk_fma_f32 v[84:85], v[98:99], v[50:51], v[84:85]
	v_pk_fma_f32 v[86:87], v[102:103], v[50:51], v[86:87]
	v_pk_add_f32 v[80:81], v[80:81], v[100:101]
	v_pk_fma_f32 v[84:85], v[100:101], v[52:53], v[84:85]
	v_pk_add_f32 v[96:97], v[52:53], v[36:37] neg_lo:[0,1] neg_hi:[0,1]
	v_pk_add_f32 v[98:99], v[54:55], v[36:37] neg_lo:[0,1] neg_hi:[0,1]
	v_pk_add_f32 v[100:101], v[50:51], v[34:35] op_sel:[1,0] op_sel_hi:[0,1] neg_lo:[0,1] neg_hi:[0,1]
	v_pk_add_f32 v[102:103], v[52:53], v[36:37] op_sel:[1,0] op_sel_hi:[0,1] neg_lo:[0,1] neg_hi:[0,1]
	v_pk_fma_f32 v[96:97], v[96:97], v[96:97], s[22:23] neg_lo:[1,0,0] neg_hi:[1,0,0]
	v_pk_fma_f32 v[98:99], v[98:99], v[98:99], s[28:29] neg_lo:[1,0,0] neg_hi:[1,0,0]
	v_pk_fma_f32 v[100:101], v[100:101], v[100:101], s[26:27] neg_lo:[1,0,0] neg_hi:[1,0,0]
	v_pk_fma_f32 v[102:103], v[102:103], v[102:103], s[26:27] neg_lo:[1,0,0] neg_hi:[1,0,0]
	v_exp_f32_e32 v96, v96
	v_exp_f32_e32 v97, v97
	v_exp_f32_e32 v98, v98
	v_exp_f32_e32 v99, v99
	v_exp_f32_e32 v100, v100
	v_exp_f32_e32 v101, v101
	v_exp_f32_e32 v102, v102
	v_exp_f32_e32 v103, v103
	v_pk_add_f32 v[82:83], v[82:83], v[96:97]
	v_pk_fma_f32 v[86:87], v[96:97], v[52:53], v[86:87]
	v_pk_add_f32 v[80:81], v[80:81], v[100:101]
	v_pk_add_f32 v[82:83], v[82:83], v[98:99]
	v_pk_fma_f32 v[86:87], v[98:99], v[54:55], v[86:87]
	v_pk_fma_f32 v[84:85], v[100:101], v[50:51], v[84:85] op_sel:[0,1,0] op_sel_hi:[1,0,1]
	v_pk_add_f32 v[82:83], v[82:83], v[102:103]
	v_pk_fma_f32 v[86:87], v[102:103], v[52:53], v[86:87] op_sel:[0,1,0] op_sel_hi:[1,0,1]
	v_pk_add_f32 v[96:97], v[48:49], v[42:43] neg_lo:[0,1] neg_hi:[0,1]
	v_pk_add_f32 v[98:99], v[50:51], v[42:43] neg_lo:[0,1] neg_hi:[0,1]
	v_pk_add_f32 v[100:101], v[52:53], v[42:43] neg_lo:[0,1] neg_hi:[0,1]
	v_pk_add_f32 v[102:103], v[50:51], v[44:45] neg_lo:[0,1] neg_hi:[0,1]
	v_pk_fma_f32 v[96:97], v[96:97], v[96:97], s[26:27] neg_lo:[1,0,0] neg_hi:[1,0,0]
	v_pk_fma_f32 v[98:99], v[98:99], v[98:99], s[20:21] neg_lo:[1,0,0] neg_hi:[1,0,0]
	v_pk_fma_f32 v[100:101], v[100:101], v[100:101], s[26:27] neg_lo:[1,0,0] neg_hi:[1,0,0]
	v_pk_fma_f32 v[102:103], v[102:103], v[102:103], s[26:27] neg_lo:[1,0,0] neg_hi:[1,0,0]
	v_exp_f32_e32 v96, v96
	v_exp_f32_e32 v97, v97
	v_exp_f32_e32 v98, v98
	v_exp_f32_e32 v99, v99
	v_exp_f32_e32 v100, v100
	v_exp_f32_e32 v101, v101
	v_exp_f32_e32 v102, v102
	v_exp_f32_e32 v103, v103
	v_pk_add_f32 v[88:89], v[88:89], v[96:97]
	v_pk_fma_f32 v[92:93], v[96:97], v[48:49], v[92:93]
	v_pk_add_f32 v[90:91], v[90:91], v[102:103]
	v_pk_add_f32 v[88:89], v[88:89], v[98:99]
	v_pk_fma_f32 v[92:93], v[98:99], v[50:51], v[92:93]
	v_pk_fma_f32 v[94:95], v[102:103], v[50:51], v[94:95]
	v_pk_add_f32 v[88:89], v[88:89], v[100:101]
	v_pk_fma_f32 v[92:93], v[100:101], v[52:53], v[92:93]
	v_pk_add_f32 v[96:97], v[52:53], v[44:45] neg_lo:[0,1] neg_hi:[0,1]
	v_pk_add_f32 v[98:99], v[54:55], v[44:45] neg_lo:[0,1] neg_hi:[0,1]
	v_pk_add_f32 v[100:101], v[50:51], v[42:43] op_sel:[1,0] op_sel_hi:[0,1] neg_lo:[0,1] neg_hi:[0,1]
	v_pk_add_f32 v[102:103], v[52:53], v[44:45] op_sel:[1,0] op_sel_hi:[0,1] neg_lo:[0,1] neg_hi:[0,1]
	v_pk_fma_f32 v[96:97], v[96:97], v[96:97], s[20:21] neg_lo:[1,0,0] neg_hi:[1,0,0]
	v_pk_fma_f32 v[98:99], v[98:99], v[98:99], s[26:27] neg_lo:[1,0,0] neg_hi:[1,0,0]
	v_pk_fma_f32 v[100:101], v[100:101], v[100:101], s[24:25] neg_lo:[1,0,0] neg_hi:[1,0,0]
	v_pk_fma_f32 v[102:103], v[102:103], v[102:103], s[24:25] neg_lo:[1,0,0] neg_hi:[1,0,0]
	v_exp_f32_e32 v96, v96
	v_exp_f32_e32 v97, v97
	v_exp_f32_e32 v98, v98
	v_exp_f32_e32 v99, v99
	v_exp_f32_e32 v100, v100
	v_exp_f32_e32 v101, v101
	v_exp_f32_e32 v102, v102
	v_exp_f32_e32 v103, v103
	v_pk_add_f32 v[90:91], v[90:91], v[96:97]
	v_pk_fma_f32 v[94:95], v[96:97], v[52:53], v[94:95]
	v_pk_add_f32 v[88:89], v[88:89], v[100:101]
	v_pk_add_f32 v[90:91], v[90:91], v[98:99]
	v_pk_fma_f32 v[94:95], v[98:99], v[54:55], v[94:95]
	v_pk_fma_f32 v[92:93], v[100:101], v[50:51], v[92:93] op_sel:[0,1,0] op_sel_hi:[1,0,1]
	v_pk_add_f32 v[90:91], v[90:91], v[102:103]
	v_pk_fma_f32 v[94:95], v[102:103], v[52:53], v[94:95] op_sel:[0,1,0] op_sel_hi:[1,0,1]
	v_sub_f32_e32 v96, v49, v34
	v_sub_f32_e32 v98, v52, v35
	v_sub_f32_e32 v100, v51, v36
	v_sub_f32_e32 v102, v54, v37
	v_sub_f32_e32 v97, v49, v42
	v_sub_f32_e32 v99, v52, v43
	v_sub_f32_e32 v101, v51, v44
	v_sub_f32_e32 v103, v54, v45
	v_fma_f32 v96, -v96, v96, s26
	v_fma_f32 v98, -v98, v98, s26
	v_fma_f32 v100, -v100, v100, s26
	v_fma_f32 v102, -v102, v102, s26
	v_fma_f32 v97, -v97, v97, s24
	v_fma_f32 v99, -v99, v99, s24
	v_fma_f32 v101, -v101, v101, s24
	v_fma_f32 v103, -v103, v103, s24
	v_exp_f32_e32 v96, v96
	v_exp_f32_e32 v98, v98
	v_exp_f32_e32 v100, v100
	v_exp_f32_e32 v102, v102
	v_exp_f32_e32 v97, v97
	v_exp_f32_e32 v99, v99
	v_exp_f32_e32 v101, v101
	v_exp_f32_e32 v103, v103
	v_add_f32_e32 v80, v80, v96
	v_fmac_f32_e32 v84, v96, v49
	v_add_f32_e32 v81, v81, v98
	v_fmac_f32_e32 v85, v98, v52
	v_add_f32_e32 v82, v82, v100
	v_fmac_f32_e32 v86, v100, v51
	v_add_f32_e32 v83, v83, v102
	v_fmac_f32_e32 v87, v102, v54
	v_add_f32_e32 v88, v88, v97
	v_fmac_f32_e32 v92, v97, v49
	v_add_f32_e32 v89, v89, v99
	v_fmac_f32_e32 v93, v99, v52
	v_add_f32_e32 v90, v90, v101
	v_fmac_f32_e32 v94, v101, v51
	v_add_f32_e32 v91, v91, v103
	v_fmac_f32_e32 v95, v103, v54
	v_rcp_f32_e32 v96, v80
	v_rcp_f32_e32 v97, v81
	v_rcp_f32_e32 v98, v82
	v_rcp_f32_e32 v99, v83
	v_pk_mul_f32 v[84:85], v[84:85], s[34:35]
	v_pk_mul_f32 v[86:87], v[86:87], s[34:35]
	v_pk_mul_f32 v[84:85], v[84:85], v[96:97]
	v_pk_mul_f32 v[86:87], v[86:87], v[98:99]
	s_nop 0
	s_nop 0
	buffer_store_dwordx4 v[84:87], v111, s[12:15], 0 offen sc1
	s_waitcnt vmcnt(3)
	s_nop 0
	v_mov_b32_dpp v56, v60 row_shr:1 row_mask:0xf bank_mask:0xf
	v_mov_b32_dpp v57, v61 row_shr:1 row_mask:0xf bank_mask:0xf
	v_mov_b32_dpp v62, v58 row_shl:1 row_mask:0xf bank_mask:0xf
	v_mov_b32_dpp v63, v59 row_shl:1 row_mask:0xf bank_mask:0xf
	v_pk_mul_f32 v[58:59], v[58:59], s[32:33]
	v_pk_mul_f32 v[60:61], v[60:61], s[32:33]
	v_cndmask_b32_e64 v57, v57, v56, vcc
	v_cndmask_b32_e64 v62, v62, v63, s[16:17]
	v_pk_mul_f32 v[56:57], v[56:57], s[32:33]
	v_pk_mul_f32 v[62:63], v[62:63], s[32:33]
	s_setprio 0
	s_nop 0
	v_pk_add_f32 v[96:97], v[56:57], v[42:43] neg_lo:[0,1] neg_hi:[0,1]
	v_pk_add_f32 v[98:99], v[58:59], v[42:43] neg_lo:[0,1] neg_hi:[0,1]
	v_pk_add_f32 v[100:101], v[60:61], v[42:43] neg_lo:[0,1] neg_hi:[0,1]
	v_pk_add_f32 v[102:103], v[58:59], v[44:45] neg_lo:[0,1] neg_hi:[0,1]
	v_pk_fma_f32 v[96:97], v[96:97], v[96:97], s[28:29] neg_lo:[1,0,0] neg_hi:[1,0,0]
	v_pk_fma_f32 v[98:99], v[98:99], v[98:99], s[22:23] neg_lo:[1,0,0] neg_hi:[1,0,0]
	v_pk_fma_f32 v[100:101], v[100:101], v[100:101], s[28:29] neg_lo:[1,0,0] neg_hi:[1,0,0]
	v_pk_fma_f32 v[102:103], v[102:103], v[102:103], s[28:29] neg_lo:[1,0,0] neg_hi:[1,0,0]
	v_exp_f32_e32 v96, v96
	v_exp_f32_e32 v97, v97
	v_exp_f32_e32 v98, v98
	v_exp_f32_e32 v99, v99
	v_exp_f32_e32 v100, v100
	v_exp_f32_e32 v101, v101
	v_exp_f32_e32 v102, v102
	v_exp_f32_e32 v103, v103
	v_pk_add_f32 v[88:89], v[88:89], v[96:97]
	v_pk_fma_f32 v[92:93], v[96:97], v[56:57], v[92:93]
	v_pk_add_f32 v[90:91], v[90:91], v[102:103]
	v_pk_add_f32 v[88:89], v[88:89], v[98:99]
	v_pk_fma_f32 v[92:93], v[98:99], v[58:59], v[92:93]
	v_pk_fma_f32 v[94:95], v[102:103], v[58:59], v[94:95]
	v_pk_add_f32 v[88:89], v[88:89], v[100:101]
	v_pk_fma_f32 v[92:93], v[100:101], v[60:61], v[92:93]
	v_pk_add_f32 v[96:97], v[60:61], v[44:45] neg_lo:[0,1] neg_hi:[0,1]
	v_pk_add_f32 v[98:99], v[62:63], v[44:45] neg_lo:[0,1] neg_hi:[0,1]
	v_pk_add_f32 v[100:101], v[58:59], v[42:43] op_sel:[1,0] op_sel_hi:[0,1] neg_lo:[0,1] neg_hi:[0,1]
	v_pk_add_f32 v[102:103], v[60:61], v[44:45] op_sel:[1,0] op_sel_hi:[0,1] neg_lo:[0,1] neg_hi:[0,1]
	v_pk_fma_f32 v[96:97], v[96:97], v[96:97], s[22:23] neg_lo:[1,0,0] neg_hi:[1,0,0]
	v_pk_fma_f32 v[98:99], v[98:99], v[98:99], s[28:29] neg_lo:[1,0,0] neg_hi:[1,0,0]
	v_pk_fma_f32 v[100:101], v[100:101], v[100:101], s[26:27] neg_lo:[1,0,0] neg_hi:[1,0,0]
	v_pk_fma_f32 v[102:103], v[102:103], v[102:103], s[26:27] neg_lo:[1,0,0] neg_hi:[1,0,0]
	v_exp_f32_e32 v96, v96
	v_exp_f32_e32 v97, v97
	v_exp_f32_e32 v98, v98
	v_exp_f32_e32 v99, v99
	v_exp_f32_e32 v100, v100
	v_exp_f32_e32 v101, v101
	v_exp_f32_e32 v102, v102
	v_exp_f32_e32 v103, v103
	v_pk_add_f32 v[90:91], v[90:91], v[96:97]
	v_pk_fma_f32 v[94:95], v[96:97], v[60:61], v[94:95]
	v_pk_add_f32 v[88:89], v[88:89], v[100:101]
	v_pk_add_f32 v[90:91], v[90:91], v[98:99]
	v_pk_fma_f32 v[94:95], v[98:99], v[62:63], v[94:95]
	v_pk_fma_f32 v[92:93], v[100:101], v[58:59], v[92:93] op_sel:[0,1,0] op_sel_hi:[1,0,1]
	v_pk_add_f32 v[90:91], v[90:91], v[102:103]
	v_pk_fma_f32 v[94:95], v[102:103], v[60:61], v[94:95] op_sel:[0,1,0] op_sel_hi:[1,0,1]
	v_sub_f32_e32 v96, v57, v42
	v_sub_f32_e32 v98, v60, v43
	v_sub_f32_e32 v100, v59, v44
	v_sub_f32_e32 v102, v62, v45
	v_fma_f32 v96, -v96, v96, s26
	v_fma_f32 v98, -v98, v98, s26
	v_fma_f32 v100, -v100, v100, s26
	v_fma_f32 v102, -v102, v102, s26
	v_exp_f32_e32 v96, v96
	v_exp_f32_e32 v98, v98
	v_exp_f32_e32 v100, v100
	v_exp_f32_e32 v102, v102
	v_add_f32_e32 v88, v88, v96
	v_fmac_f32_e32 v92, v96, v57
	v_add_f32_e32 v89, v89, v98
	v_fmac_f32_e32 v93, v98, v60
	v_add_f32_e32 v90, v90, v100
	v_fmac_f32_e32 v94, v100, v59
	v_add_f32_e32 v91, v91, v102
	v_fmac_f32_e32 v95, v102, v62
	v_rcp_f32_e32 v96, v88
	v_rcp_f32_e32 v97, v89
	v_rcp_f32_e32 v98, v90
	v_rcp_f32_e32 v99, v91
	v_pk_mul_f32 v[92:93], v[92:93], s[34:35]
	v_pk_mul_f32 v[94:95], v[94:95], s[34:35]
	v_pk_mul_f32 v[92:93], v[92:93], v[96:97]
	v_pk_mul_f32 v[94:95], v[94:95], v[98:99]
	s_nop 0
	s_nop 0
	buffer_store_dwordx4 v[92:95], v111, s[12:15], 0 offen offset:2048 sc1
	s_endpgm

	.amdhsa_kernel _Z16bilateral_kernelPKfS0_Pf
		.amdhsa_group_segment_fixed_size 0
		.amdhsa_private_segment_fixed_size 0
		.amdhsa_kernarg_size 24
		.amdhsa_user_sgpr_count 2
		.amdhsa_user_sgpr_dispatch_ptr 0
		.amdhsa_user_sgpr_queue_ptr 0
		.amdhsa_user_sgpr_kernarg_segment_ptr 1
		.amdhsa_user_sgpr_dispatch_id 0
		.amdhsa_user_sgpr_kernarg_preload_length 0
		.amdhsa_user_sgpr_kernarg_preload_offset 0
		.amdhsa_user_sgpr_private_segment_size 0
		.amdhsa_uses_dynamic_stack 0
		.amdhsa_enable_private_segment 0
		.amdhsa_system_sgpr_workgroup_id_x 1
		.amdhsa_system_sgpr_workgroup_id_y 0
		.amdhsa_system_sgpr_workgroup_id_z 0
		.amdhsa_system_sgpr_workgroup_info 0
		.amdhsa_system_vgpr_workitem_id 0
		.amdhsa_next_free_vgpr 112
		.amdhsa_next_free_sgpr 40
		.amdhsa_accum_offset 112
		.amdhsa_reserve_vcc 1
		.amdhsa_float_round_mode_32 0
		.amdhsa_float_round_mode_16_64 0
		.amdhsa_float_denorm_mode_32 3
		.amdhsa_float_denorm_mode_16_64 3
		.amdhsa_dx10_clamp 1
		.amdhsa_ieee_mode 1
		.amdhsa_fp16_overflow 0
		.amdhsa_tg_split 0
		.amdhsa_exception_fp_ieee_invalid_op 0
		.amdhsa_exception_fp_denorm_src 0
		.amdhsa_exception_fp_ieee_div_zero 0
		.amdhsa_exception_fp_ieee_overflow 0
		.amdhsa_exception_fp_ieee_underflow 0
		.amdhsa_exception_fp_ieee_inexact 0
		.amdhsa_exception_int_div_zero 0
	.end_amdhsa_kernel

amdhsa.kernels:
  - .agpr_count:     0
    .args:
      - .actual_access:  read_only
        .address_space:  global
        .offset:         0
        .size:           8
        .value_kind:     global_buffer
      - .actual_access:  read_only
        .address_space:  global
        .offset:         8
        .size:           8
        .value_kind:     global_buffer
      - .actual_access:  write_only
        .address_space:  global
        .offset:         16
        .size:           8
        .value_kind:     global_buffer
    .group_segment_fixed_size: 0
    .kernarg_segment_align: 8
    .kernarg_segment_size: 24
    .language:       OpenCL C
    .language_version:
      - 2
      - 0
    .max_flat_workgroup_size: 256
    .name:           _Z16bilateral_kernelPKfS0_Pf
    .private_segment_fixed_size: 0
    .sgpr_count:     46
    .sgpr_spill_count: 0
    .symbol:         _Z16bilateral_kernelPKfS0_Pf.kd
    .uniform_work_group_size: 1
    .uses_dynamic_stack: false
    .vgpr_count:     112
    .vgpr_spill_count: 0
    .wavefront_size: 64
